# removed s_nop 15 pairs after fp8 K-loops (MFMA->VALU distance already met by intervening code)
# speedup vs baseline: 1.0185x; 1.0002x over previous
.LBB0_669:
	v_mov_b32_e32 v0, v215
	s_mul_i32 s30, s36, 0x2200000
	v_readfirstlane_b32 s71, v0
	s_bfe_u32 s28, s71, 0x20006
	s_mul_hi_i32 s29, s36, 0x2200000
	s_add_u32 s82, s16, s30
	v_and_b32_e32 v11, 15, v0
	v_bfe_u32 v0, v0, 4, 2
	s_addc_u32 s83, s17, s29
	s_lshl_b32 s73, s28, 5
	v_lshlrev_b32_e32 v10, 3, v0
	s_cmp_gt_i32 s36, 11
	s_mov_b64 s[50:51], -1
	s_mov_b32 s37, s8
	s_cbranch_scc0 .LBB0_671
	s_ashr_i32 s75, s74, 31
	s_lshl_b64 s[30:31], s[74:75], 16
	s_add_u32 s30, s82, s30
	s_addc_u32 s31, s83, s31
	s_and_b32 s29, s71, 0xfffff00
	s_lshl_b32 s28, s28, 6
	s_or_b32 s28, s28, s29
	v_lshlrev_b32_e32 v0, 4, v0
	v_or3_b32 v0, s28, v0, v11
	s_lshl_b32 s28, s36, 8
	s_add_i32 s28, s28, 0x7ffff400
	s_and_b32 s28, s28, 0x7ffffc00
	s_mov_b32 s29, s5
	v_lshlrev_b32_e32 v0, 4, v0
	s_lshl_b64 s[28:29], s[28:29], 2
	v_ashrrev_i32_e32 v1, 31, v0
	s_add_u32 s28, s15, s28
	v_lshl_add_u64 v[8:9], s[30:31], 0, v[0:1]
	s_addc_u32 s29, s25, s29
	s_lshl_b32 s30, s36, 10
	s_and_b32 s30, s30, 0xc00
	s_add_u32 s28, s28, s30
	s_addc_u32 s29, s29, 0
	s_lshl_b32 s30, s73, 2
	s_add_u32 s96, s28, s30
	s_addc_u32 s97, s29, 0
	v_lshlrev_b32_e32 v12, 2, v10
	global_load_dwordx4 v[0:3], v12, s[96:97] offset:16
	global_load_dwordx4 v[4:7], v12, s[96:97]
	s_mov_b32 s28, 0xa000
	s_mov_b64 s[50:51], 0
	s_waitcnt vmcnt(0)
	v_mul_f32_e32 v0, 0xbfb8aa3b, v0
	v_mul_f32_e32 v4, 0xbfb8aa3b, v4
	v_fmamk_f32 v13, v158, 0xbfb8aa3b, v4
	v_mul_f32_e32 v5, 0xbfb8aa3b, v5
	v_exp_f32_e32 v13, v13
	v_fmamk_f32 v17, v159, 0xbfb8aa3b, v5
	v_exp_f32_e32 v17, v17
	v_fmamk_f32 v14, v154, 0xbfb8aa3b, v0
	v_fmamk_f32 v13, v13, 0x3b808081, v198
	v_rcp_f32_e32 v13, v13
	v_fmamk_f32 v17, v17, 0x3b808081, v198
	v_rcp_f32_e32 v17, v17
	v_mul_f32_e32 v1, 0xbfb8aa3b, v1
	v_cvt_pk_u8_f32 v13, v13, 0, 0
	v_exp_f32_e32 v14, v14
	v_cvt_pk_u8_f32 v13, v17, 1, v13
	v_fmamk_f32 v17, v155, 0xbfb8aa3b, v1
	v_exp_f32_e32 v17, v17
	v_fmamk_f32 v14, v14, 0x3b808081, v198
	v_rcp_f32_e32 v14, v14
	v_fmamk_f32 v15, v150, 0xbfb8aa3b, v4
	v_fmamk_f32 v17, v17, 0x3b808081, v198
	v_rcp_f32_e32 v17, v17
	v_cvt_pk_u8_f32 v14, v14, 0, 0
	v_exp_f32_e32 v15, v15
	v_fmamk_f32 v16, v146, 0xbfb8aa3b, v0
	v_cvt_pk_u8_f32 v14, v17, 1, v14
	v_fmamk_f32 v17, v151, 0xbfb8aa3b, v5
	v_exp_f32_e32 v17, v17
	v_fmamk_f32 v15, v15, 0x3b808081, v198
	v_rcp_f32_e32 v15, v15
	v_exp_f32_e32 v16, v16
	v_fmamk_f32 v17, v17, 0x3b808081, v198
	v_rcp_f32_e32 v17, v17
	v_cvt_pk_u8_f32 v15, v15, 0, 0
	v_fmamk_f32 v16, v16, 0x3b808081, v198
	v_rcp_f32_e32 v16, v16
	v_cvt_pk_u8_f32 v15, v17, 1, v15
	v_fmamk_f32 v17, v147, 0xbfb8aa3b, v1
	v_exp_f32_e32 v17, v17
	v_cvt_pk_u8_f32 v16, v16, 0, 0
	v_mul_f32_e32 v6, 0xbfb8aa3b, v6
	v_mul_f32_e32 v2, 0xbfb8aa3b, v2
	v_fmamk_f32 v17, v17, 0x3b808081, v198
	v_rcp_f32_e32 v17, v17
	v_mul_f32_e32 v7, 0xbfb8aa3b, v7
	v_mul_f32_e32 v3, 0xbfb8aa3b, v3
	v_cvt_pk_u8_f32 v16, v17, 1, v16
	v_fmamk_f32 v17, v160, 0xbfb8aa3b, v6
	v_exp_f32_e32 v17, v17
	s_nop 0
	v_fmamk_f32 v17, v17, 0x3b808081, v198
	v_rcp_f32_e32 v17, v17
	s_nop 0
	v_cvt_pk_u8_f32 v13, v17, 2, v13
	v_fmamk_f32 v17, v156, 0xbfb8aa3b, v2
	v_exp_f32_e32 v17, v17
	s_nop 0
	v_fmamk_f32 v17, v17, 0x3b808081, v198
	v_rcp_f32_e32 v17, v17
	s_nop 0
	v_cvt_pk_u8_f32 v14, v17, 2, v14
	v_fmamk_f32 v17, v152, 0xbfb8aa3b, v6
	v_exp_f32_e32 v17, v17
	s_nop 0
	v_fmamk_f32 v17, v17, 0x3b808081, v198
	v_rcp_f32_e32 v17, v17
	s_nop 0
	v_cvt_pk_u8_f32 v15, v17, 2, v15
	v_fmamk_f32 v17, v148, 0xbfb8aa3b, v2
	v_exp_f32_e32 v17, v17
	s_nop 0
	v_fmamk_f32 v17, v17, 0x3b808081, v198
	v_rcp_f32_e32 v17, v17
	s_nop 0
	v_cvt_pk_u8_f32 v16, v17, 2, v16
	v_fmamk_f32 v17, v161, 0xbfb8aa3b, v7
	v_exp_f32_e32 v17, v17
	s_nop 0
	v_fmamk_f32 v17, v17, 0x3b808081, v198
	v_rcp_f32_e32 v17, v17
	s_nop 0
	v_cvt_pk_u8_f32 v13, v17, 3, v13
	v_fmamk_f32 v17, v157, 0xbfb8aa3b, v3
	v_exp_f32_e32 v17, v17
	s_nop 0
	v_fmamk_f32 v17, v17, 0x3b808081, v198
	v_rcp_f32_e32 v17, v17
	s_nop 0
	v_cvt_pk_u8_f32 v17, v17, 3, v14
	v_fmamk_f32 v14, v153, 0xbfb8aa3b, v7
	v_exp_f32_e32 v14, v14
	s_nop 0
	v_fmamk_f32 v14, v14, 0x3b808081, v198
	v_rcp_f32_e32 v14, v14
	s_nop 0
	v_cvt_pk_u8_f32 v18, v14, 3, v15
	v_fmamk_f32 v14, v149, 0xbfb8aa3b, v3
	v_exp_f32_e32 v14, v14
	v_or_b32_e32 v15, 0x1010101, v17
	v_fmamk_f32 v14, v14, 0x3b808081, v198
	v_rcp_f32_e32 v14, v14
	s_nop 0
	v_cvt_pk_u8_f32 v19, v14, 3, v16
	v_or_b32_e32 v14, 0x1010101, v13
	v_or_b32_e32 v16, 0x1010101, v18
	v_or_b32_e32 v17, 0x1010101, v19
	v_fmamk_f32 v13, v134, 0xbfb8aa3b, v4
	global_store_dwordx4 v[8:9], v[14:17], off
	v_exp_f32_e32 v13, v13
	s_nop 0
	v_fmamk_f32 v17, v135, 0xbfb8aa3b, v5
	v_exp_f32_e32 v17, v17
	v_fmamk_f32 v13, v13, 0x3b808081, v198
	v_rcp_f32_e32 v13, v13
	v_fmamk_f32 v14, v130, 0xbfb8aa3b, v0
	v_fmamk_f32 v17, v17, 0x3b808081, v198
	v_rcp_f32_e32 v17, v17
	v_cvt_pk_u8_f32 v13, v13, 0, 0
	v_exp_f32_e32 v14, v14
	v_fmamk_f32 v15, v118, 0xbfb8aa3b, v4
	v_cvt_pk_u8_f32 v13, v17, 1, v13
	v_fmamk_f32 v17, v131, 0xbfb8aa3b, v1
	v_exp_f32_e32 v17, v17
	v_fmamk_f32 v14, v14, 0x3b808081, v198
	v_rcp_f32_e32 v14, v14
	v_exp_f32_e32 v15, v15
	v_fmamk_f32 v17, v17, 0x3b808081, v198
	v_rcp_f32_e32 v17, v17
	v_cvt_pk_u8_f32 v14, v14, 0, 0
	v_fmamk_f32 v15, v15, 0x3b808081, v198
	v_rcp_f32_e32 v15, v15
	v_cvt_pk_u8_f32 v14, v17, 1, v14
	v_fmamk_f32 v17, v119, 0xbfb8aa3b, v5
	v_exp_f32_e32 v17, v17
	v_cvt_pk_u8_f32 v15, v15, 0, 0
	v_fmamk_f32 v16, v114, 0xbfb8aa3b, v0
	v_exp_f32_e32 v16, v16
	v_fmamk_f32 v17, v17, 0x3b808081, v198
	v_rcp_f32_e32 v17, v17
	v_fmamk_f32 v16, v16, 0x3b808081, v198
	v_rcp_f32_e32 v16, v16
	v_cvt_pk_u8_f32 v15, v17, 1, v15
	v_fmamk_f32 v17, v115, 0xbfb8aa3b, v1
	v_exp_f32_e32 v17, v17
	v_cvt_pk_u8_f32 v16, v16, 0, 0
	v_fmamk_f32 v17, v17, 0x3b808081, v198
	v_rcp_f32_e32 v17, v17
	s_nop 0
	v_cvt_pk_u8_f32 v16, v17, 1, v16
	v_fmamk_f32 v17, v136, 0xbfb8aa3b, v6
	v_exp_f32_e32 v17, v17
	s_nop 0
	v_fmamk_f32 v17, v17, 0x3b808081, v198
	v_rcp_f32_e32 v17, v17
	s_nop 0
	v_cvt_pk_u8_f32 v13, v17, 2, v13
	v_fmamk_f32 v17, v132, 0xbfb8aa3b, v2
	v_exp_f32_e32 v17, v17
	s_nop 0
	v_fmamk_f32 v17, v17, 0x3b808081, v198
	v_rcp_f32_e32 v17, v17
	s_nop 0
	v_cvt_pk_u8_f32 v14, v17, 2, v14
	v_fmamk_f32 v17, v120, 0xbfb8aa3b, v6
	v_exp_f32_e32 v17, v17
	s_nop 0
	v_fmamk_f32 v17, v17, 0x3b808081, v198
	v_rcp_f32_e32 v17, v17
	s_nop 0
	v_cvt_pk_u8_f32 v15, v17, 2, v15
	v_fmamk_f32 v17, v116, 0xbfb8aa3b, v2
	v_exp_f32_e32 v17, v17
	s_nop 0
	v_fmamk_f32 v17, v17, 0x3b808081, v198
	v_rcp_f32_e32 v17, v17
	s_nop 0
	v_cvt_pk_u8_f32 v16, v17, 2, v16
	v_fmamk_f32 v17, v137, 0xbfb8aa3b, v7
	v_exp_f32_e32 v17, v17
	s_nop 0
	v_fmamk_f32 v17, v17, 0x3b808081, v198
	v_rcp_f32_e32 v17, v17
	s_nop 0
	v_cvt_pk_u8_f32 v13, v17, 3, v13
	v_fmamk_f32 v17, v133, 0xbfb8aa3b, v3
	v_exp_f32_e32 v17, v17
	s_nop 0
	v_fmamk_f32 v17, v17, 0x3b808081, v198
	v_rcp_f32_e32 v17, v17
	s_nop 0
	v_cvt_pk_u8_f32 v17, v17, 3, v14
	v_fmamk_f32 v14, v121, 0xbfb8aa3b, v7
	v_exp_f32_e32 v14, v14
	s_nop 0
	v_fmamk_f32 v14, v14, 0x3b808081, v198
	v_rcp_f32_e32 v14, v14
	s_nop 0
	v_cvt_pk_u8_f32 v18, v14, 3, v15
	v_fmamk_f32 v14, v117, 0xbfb8aa3b, v3
	v_exp_f32_e32 v14, v14
	v_or_b32_e32 v15, 0x1010101, v17
	v_fmamk_f32 v14, v14, 0x3b808081, v198
	v_rcp_f32_e32 v14, v14
	s_nop 0
	v_cvt_pk_u8_f32 v19, v14, 3, v16
	v_or_b32_e32 v16, 0x1010101, v18
	v_add_co_u32_e32 v18, vcc, s59, v8
	v_or_b32_e32 v14, 0x1010101, v13
	v_or_b32_e32 v17, 0x1010101, v19
	v_addc_co_u32_e32 v19, vcc, 0, v9, vcc
	v_fmamk_f32 v13, v92, 0xbfb8aa3b, v4
	global_store_dwordx4 v[18:19], v[14:17], off
	v_exp_f32_e32 v13, v13
	s_nop 0
	v_fmamk_f32 v17, v93, 0xbfb8aa3b, v5
	v_exp_f32_e32 v17, v17
	v_fmamk_f32 v13, v13, 0x3b808081, v198
	v_rcp_f32_e32 v13, v13
	v_fmamk_f32 v14, v88, 0xbfb8aa3b, v0
	v_fmamk_f32 v17, v17, 0x3b808081, v198
	v_rcp_f32_e32 v17, v17
	v_cvt_pk_u8_f32 v13, v13, 0, 0
	v_exp_f32_e32 v14, v14
	v_fmamk_f32 v15, v84, 0xbfb8aa3b, v4
	v_cvt_pk_u8_f32 v13, v17, 1, v13
	v_fmamk_f32 v17, v89, 0xbfb8aa3b, v1
	v_exp_f32_e32 v17, v17
	v_fmamk_f32 v14, v14, 0x3b808081, v198
	v_rcp_f32_e32 v14, v14
	v_exp_f32_e32 v15, v15
	v_fmamk_f32 v17, v17, 0x3b808081, v198
	v_rcp_f32_e32 v17, v17
	v_cvt_pk_u8_f32 v14, v14, 0, 0
	v_fmamk_f32 v15, v15, 0x3b808081, v198
	v_rcp_f32_e32 v15, v15
	v_cvt_pk_u8_f32 v14, v17, 1, v14
	v_fmamk_f32 v17, v85, 0xbfb8aa3b, v5
	v_exp_f32_e32 v17, v17
	v_cvt_pk_u8_f32 v15, v15, 0, 0
	v_fmamk_f32 v16, v80, 0xbfb8aa3b, v0
	v_exp_f32_e32 v16, v16
	v_fmamk_f32 v17, v17, 0x3b808081, v198
	v_rcp_f32_e32 v17, v17
	v_fmamk_f32 v16, v16, 0x3b808081, v198
	v_rcp_f32_e32 v16, v16
	v_cvt_pk_u8_f32 v15, v17, 1, v15
	v_fmamk_f32 v17, v81, 0xbfb8aa3b, v1
	v_exp_f32_e32 v17, v17
	v_cvt_pk_u8_f32 v16, v16, 0, 0
	v_fmamk_f32 v17, v17, 0x3b808081, v198
	v_rcp_f32_e32 v17, v17
	s_nop 0
	v_cvt_pk_u8_f32 v16, v17, 1, v16
	v_fmamk_f32 v17, v94, 0xbfb8aa3b, v6
	v_exp_f32_e32 v17, v17
	s_nop 0
	v_fmamk_f32 v17, v17, 0x3b808081, v198
	v_rcp_f32_e32 v17, v17
	s_nop 0
	v_cvt_pk_u8_f32 v13, v17, 2, v13
	v_fmamk_f32 v17, v90, 0xbfb8aa3b, v2
	v_exp_f32_e32 v17, v17
	s_nop 0
	v_fmamk_f32 v17, v17, 0x3b808081, v198
	v_rcp_f32_e32 v17, v17
	s_nop 0
	v_cvt_pk_u8_f32 v14, v17, 2, v14
	v_fmamk_f32 v17, v86, 0xbfb8aa3b, v6
	v_exp_f32_e32 v17, v17
	s_nop 0
	v_fmamk_f32 v17, v17, 0x3b808081, v198
	v_rcp_f32_e32 v17, v17
	s_nop 0
	v_cvt_pk_u8_f32 v15, v17, 2, v15
	v_fmamk_f32 v17, v82, 0xbfb8aa3b, v2
	v_exp_f32_e32 v17, v17
	s_nop 0
	v_fmamk_f32 v17, v17, 0x3b808081, v198
	v_rcp_f32_e32 v17, v17
	s_nop 0
	v_cvt_pk_u8_f32 v16, v17, 2, v16
	v_fmamk_f32 v17, v95, 0xbfb8aa3b, v7
	v_exp_f32_e32 v17, v17
	s_nop 0
	v_fmamk_f32 v17, v17, 0x3b808081, v198
	v_rcp_f32_e32 v17, v17
	s_nop 0
	v_cvt_pk_u8_f32 v13, v17, 3, v13
	v_fmamk_f32 v17, v91, 0xbfb8aa3b, v3
	v_exp_f32_e32 v17, v17
	s_nop 0
	v_fmamk_f32 v17, v17, 0x3b808081, v198
	v_rcp_f32_e32 v17, v17
	s_nop 0
	v_cvt_pk_u8_f32 v17, v17, 3, v14
	v_fmamk_f32 v14, v87, 0xbfb8aa3b, v7
	v_exp_f32_e32 v14, v14
	s_nop 0
	v_fmamk_f32 v14, v14, 0x3b808081, v198
	v_rcp_f32_e32 v14, v14
	s_nop 0
	v_cvt_pk_u8_f32 v18, v14, 3, v15
	v_fmamk_f32 v14, v83, 0xbfb8aa3b, v3
	v_exp_f32_e32 v14, v14
	v_or_b32_e32 v15, 0x1010101, v17
	v_fmamk_f32 v14, v14, 0x3b808081, v198
	v_rcp_f32_e32 v14, v14
	s_nop 0
	v_cvt_pk_u8_f32 v19, v14, 3, v16
	v_or_b32_e32 v16, 0x1010101, v18
	v_add_co_u32_e32 v18, vcc, s62, v8
	v_or_b32_e32 v14, 0x1010101, v13
	v_or_b32_e32 v17, 0x1010101, v19
	v_addc_co_u32_e32 v19, vcc, 0, v9, vcc
	v_fmamk_f32 v13, v68, 0xbfb8aa3b, v4
	global_store_dwordx4 v[18:19], v[14:17], off
	v_exp_f32_e32 v13, v13
	v_fmac_f32_e32 v4, 0xbfb8aa3b, v52
	v_fmamk_f32 v15, v69, 0xbfb8aa3b, v5
	v_exp_f32_e32 v4, v4
	v_exp_f32_e32 v15, v15
	v_fmac_f32_e32 v5, 0xbfb8aa3b, v53
	v_exp_f32_e32 v5, v5
	v_fmamk_f32 v13, v13, 0x3b808081, v198
	v_rcp_f32_e32 v13, v13
	v_fmamk_f32 v4, v4, 0x3b808081, v198
	v_fmamk_f32 v15, v15, 0x3b808081, v198
	v_rcp_f32_e32 v4, v4
	v_rcp_f32_e32 v15, v15
	v_fmamk_f32 v5, v5, 0x3b808081, v198
	v_rcp_f32_e32 v5, v5
	v_cvt_pk_u8_f32 v13, v13, 0, 0
	v_fmamk_f32 v14, v64, 0xbfb8aa3b, v0
	v_fmac_f32_e32 v0, 0xbfb8aa3b, v48
	v_cvt_pk_u8_f32 v4, v4, 0, 0
	v_exp_f32_e32 v0, v0
	v_cvt_pk_u8_f32 v13, v15, 1, v13
	v_fmamk_f32 v15, v65, 0xbfb8aa3b, v1
	v_fmac_f32_e32 v1, 0xbfb8aa3b, v49
	v_cvt_pk_u8_f32 v4, v5, 1, v4
	v_exp_f32_e32 v1, v1
	v_fmamk_f32 v5, v66, 0xbfb8aa3b, v2
	v_fmac_f32_e32 v2, 0xbfb8aa3b, v50
	v_exp_f32_e32 v2, v2
	v_fmamk_f32 v0, v0, 0x3b808081, v198
	v_rcp_f32_e32 v0, v0
	v_fmamk_f32 v1, v1, 0x3b808081, v198
	v_rcp_f32_e32 v1, v1
	v_fmamk_f32 v2, v2, 0x3b808081, v198
	v_rcp_f32_e32 v2, v2
	v_cvt_pk_u8_f32 v0, v0, 0, 0
	v_cvt_pk_u8_f32 v0, v1, 1, v0
	v_fmamk_f32 v1, v70, 0xbfb8aa3b, v6
	v_exp_f32_e32 v1, v1
	v_cvt_pk_u8_f32 v0, v2, 2, v0
	v_fmamk_f32 v2, v71, 0xbfb8aa3b, v7
	v_exp_f32_e32 v2, v2
	v_fmamk_f32 v1, v1, 0x3b808081, v198
	v_rcp_f32_e32 v1, v1
	v_exp_f32_e32 v14, v14
	v_fmamk_f32 v2, v2, 0x3b808081, v198
	v_rcp_f32_e32 v2, v2
	v_exp_f32_e32 v15, v15
	v_cvt_pk_u8_f32 v1, v1, 2, v13
	v_exp_f32_e32 v5, v5
	v_cvt_pk_u8_f32 v1, v2, 3, v1
	v_fmamk_f32 v2, v67, 0xbfb8aa3b, v3
	v_exp_f32_e32 v2, v2
	v_fmamk_f32 v14, v14, 0x3b808081, v198
	v_rcp_f32_e32 v14, v14
	v_fmamk_f32 v15, v15, 0x3b808081, v198
	v_rcp_f32_e32 v15, v15
	v_fmamk_f32 v5, v5, 0x3b808081, v198
	v_rcp_f32_e32 v5, v5
	v_fmamk_f32 v2, v2, 0x3b808081, v198
	v_rcp_f32_e32 v2, v2
	v_cvt_pk_u8_f32 v14, v14, 0, 0
	v_cvt_pk_u8_f32 v14, v15, 1, v14
	v_fmac_f32_e32 v6, 0xbfb8aa3b, v54
	v_cvt_pk_u8_f32 v5, v5, 2, v14
	v_exp_f32_e32 v6, v6
	v_fmac_f32_e32 v7, 0xbfb8aa3b, v55
	v_cvt_pk_u8_f32 v2, v2, 3, v5
	v_exp_f32_e32 v5, v7
	v_fmac_f32_e32 v3, 0xbfb8aa3b, v51
	v_exp_f32_e32 v3, v3
	v_fmamk_f32 v6, v6, 0x3b808081, v198
	v_rcp_f32_e32 v6, v6
	v_fmamk_f32 v5, v5, 0x3b808081, v198
	v_rcp_f32_e32 v5, v5
	v_fmamk_f32 v3, v3, 0x3b808081, v198
	v_rcp_f32_e32 v3, v3
	v_cvt_pk_u8_f32 v4, v6, 2, v4
	v_cvt_pk_u8_f32 v4, v5, 3, v4
	v_cvt_pk_u8_f32 v3, v3, 3, v0
	v_or_b32_e32 v0, 0x1010101, v1
	v_or_b32_e32 v1, 0x1010101, v2
	v_or_b32_e32 v2, 0x1010101, v4
	v_add_co_u32_e32 v4, vcc, s89, v8
	v_or_b32_e32 v3, 0x1010101, v3
	s_nop 0
	v_addc_co_u32_e32 v5, vcc, 0, v9, vcc
	global_store_dwordx4 v[4:5], v[0:3], off
	global_load_dwordx4 v[0:3], v12, s[96:97] offset:528
	s_nop 0
	global_load_dwordx4 v[4:7], v12, s[96:97] offset:512
	s_waitcnt vmcnt(1)
	v_mul_f32_e32 v12, 0xbfb8aa3b, v0
	v_fmamk_f32 v0, v138, 0xbfb8aa3b, v12
	v_exp_f32_e32 v0, v0
	s_waitcnt vmcnt(0)
	v_mul_f32_e32 v13, 0xbfb8aa3b, v4
	v_fmamk_f32 v4, v142, 0xbfb8aa3b, v13
	v_exp_f32_e32 v4, v4
	v_fmamk_f32 v0, v0, 0x3b808081, v198
	v_rcp_f32_e32 v0, v0
	v_mul_f32_e32 v1, 0xbfb8aa3b, v1
	v_fmamk_f32 v4, v4, 0x3b808081, v198
	v_rcp_f32_e32 v4, v4
	v_cvt_pk_u8_f32 v14, v0, 0, 0
	v_fmamk_f32 v0, v126, 0xbfb8aa3b, v13
	v_exp_f32_e32 v0, v0
	v_cvt_pk_u8_f32 v4, v4, 0, 0
	v_mul_f32_e32 v3, 0xbfb8aa3b, v3
	v_fmamk_f32 v0, v0, 0x3b808081, v198
	v_rcp_f32_e32 v0, v0
	s_nop 0
	v_cvt_pk_u8_f32 v15, v0, 0, 0
	v_fmamk_f32 v0, v122, 0xbfb8aa3b, v12
	v_exp_f32_e32 v0, v0
	s_nop 0
	v_fmamk_f32 v0, v0, 0x3b808081, v198
	v_rcp_f32_e32 v0, v0
	s_nop 0
	v_cvt_pk_u8_f32 v16, v0, 0, 0
	v_mul_f32_e32 v0, 0xbfb8aa3b, v5
	v_fmamk_f32 v5, v143, 0xbfb8aa3b, v0
	v_exp_f32_e32 v5, v5
	s_nop 0
	v_fmamk_f32 v5, v5, 0x3b808081, v198
	v_rcp_f32_e32 v5, v5
	s_nop 0
	v_cvt_pk_u8_f32 v5, v5, 1, v4
	v_fmamk_f32 v4, v139, 0xbfb8aa3b, v1
	v_exp_f32_e32 v4, v4
	s_nop 0
	v_fmamk_f32 v4, v4, 0x3b808081, v198
	v_rcp_f32_e32 v4, v4
	s_nop 0
	v_cvt_pk_u8_f32 v14, v4, 1, v14
	v_fmamk_f32 v4, v127, 0xbfb8aa3b, v0
	v_exp_f32_e32 v4, v4
	s_nop 0
	v_fmamk_f32 v4, v4, 0x3b808081, v198
	v_rcp_f32_e32 v4, v4
	s_nop 0
	v_cvt_pk_u8_f32 v15, v4, 1, v15
	v_fmamk_f32 v4, v123, 0xbfb8aa3b, v1
	v_exp_f32_e32 v4, v4
	s_nop 0
	v_fmamk_f32 v4, v4, 0x3b808081, v198
	v_rcp_f32_e32 v4, v4
	s_nop 0
	v_cvt_pk_u8_f32 v16, v4, 1, v16
	v_mul_f32_e32 v4, 0xbfb8aa3b, v6
	v_fmamk_f32 v6, v144, 0xbfb8aa3b, v4
	v_exp_f32_e32 v6, v6
	s_nop 0
	v_fmamk_f32 v6, v6, 0x3b808081, v198
	v_rcp_f32_e32 v6, v6
	s_nop 0
	v_cvt_pk_u8_f32 v6, v6, 2, v5
	v_mul_f32_e32 v5, 0xbfb8aa3b, v2
	v_fmamk_f32 v2, v140, 0xbfb8aa3b, v5
	v_exp_f32_e32 v2, v2
	s_nop 0
	v_fmamk_f32 v2, v2, 0x3b808081, v198
	v_rcp_f32_e32 v2, v2
	s_nop 0
	v_cvt_pk_u8_f32 v14, v2, 2, v14
	v_fmamk_f32 v2, v128, 0xbfb8aa3b, v4
	v_exp_f32_e32 v2, v2
	s_nop 0
	v_fmamk_f32 v2, v2, 0x3b808081, v198
	v_rcp_f32_e32 v2, v2
	s_nop 0
	v_cvt_pk_u8_f32 v15, v2, 2, v15
	v_fmamk_f32 v2, v124, 0xbfb8aa3b, v5
	v_exp_f32_e32 v2, v2
	s_nop 0
	v_fmamk_f32 v2, v2, 0x3b808081, v198
	v_rcp_f32_e32 v2, v2
	s_nop 0
	v_cvt_pk_u8_f32 v16, v2, 2, v16
	v_mul_f32_e32 v2, 0xbfb8aa3b, v7
	v_fmamk_f32 v7, v145, 0xbfb8aa3b, v2
	v_exp_f32_e32 v7, v7
	s_nop 0
	v_fmamk_f32 v7, v7, 0x3b808081, v198
	v_rcp_f32_e32 v7, v7
	s_nop 0
	v_cvt_pk_u8_f32 v6, v7, 3, v6
	v_fmamk_f32 v7, v141, 0xbfb8aa3b, v3
	v_exp_f32_e32 v7, v7
	s_nop 0
	v_fmamk_f32 v7, v7, 0x3b808081, v198
	v_rcp_f32_e32 v7, v7
	s_nop 0
	v_cvt_pk_u8_f32 v7, v7, 3, v14
	v_fmamk_f32 v14, v129, 0xbfb8aa3b, v2
	v_exp_f32_e32 v14, v14
	s_nop 0
	v_fmamk_f32 v14, v14, 0x3b808081, v198
	v_rcp_f32_e32 v14, v14
	s_nop 0
	v_cvt_pk_u8_f32 v17, v14, 3, v15
	v_fmamk_f32 v14, v125, 0xbfb8aa3b, v3
	v_exp_f32_e32 v14, v14
	v_or_b32_e32 v15, 0x1010101, v7
	v_fmamk_f32 v14, v14, 0x3b808081, v198
	v_rcp_f32_e32 v14, v14
	s_nop 0
	v_cvt_pk_u8_f32 v18, v14, 3, v16
	v_or_b32_e32 v14, 0x1010101, v6
	v_add_co_u32_e32 v6, vcc, s24, v8
	v_or_b32_e32 v16, 0x1010101, v17
	v_or_b32_e32 v17, 0x1010101, v18
	v_addc_co_u32_e32 v7, vcc, 0, v9, vcc
	global_store_dwordx4 v[6:7], v[14:17], off
	v_fmamk_f32 v6, v108, 0xbfb8aa3b, v13
	v_exp_f32_e32 v6, v6
	v_fmamk_f32 v16, v109, 0xbfb8aa3b, v0
	v_exp_f32_e32 v16, v16
	v_fmamk_f32 v7, v104, 0xbfb8aa3b, v12
	v_fmamk_f32 v6, v6, 0x3b808081, v198
	v_rcp_f32_e32 v6, v6
	v_fmamk_f32 v16, v16, 0x3b808081, v198
	v_rcp_f32_e32 v16, v16
	v_exp_f32_e32 v7, v7
	v_cvt_pk_u8_f32 v6, v6, 0, 0
	v_fmamk_f32 v14, v100, 0xbfb8aa3b, v13
	v_cvt_pk_u8_f32 v6, v16, 1, v6
	v_fmamk_f32 v16, v105, 0xbfb8aa3b, v1
	v_exp_f32_e32 v16, v16
	v_fmamk_f32 v7, v7, 0x3b808081, v198
	v_rcp_f32_e32 v7, v7
	v_exp_f32_e32 v14, v14
	v_fmamk_f32 v16, v16, 0x3b808081, v198
	v_rcp_f32_e32 v16, v16
	v_cvt_pk_u8_f32 v7, v7, 0, 0
	v_fmamk_f32 v14, v14, 0x3b808081, v198
	v_rcp_f32_e32 v14, v14
	v_cvt_pk_u8_f32 v7, v16, 1, v7
	v_fmamk_f32 v16, v101, 0xbfb8aa3b, v0
	v_exp_f32_e32 v16, v16
	v_cvt_pk_u8_f32 v14, v14, 0, 0
	v_fmamk_f32 v15, v96, 0xbfb8aa3b, v12
	v_exp_f32_e32 v15, v15
	v_fmamk_f32 v16, v16, 0x3b808081, v198
	v_rcp_f32_e32 v16, v16
	v_fmamk_f32 v15, v15, 0x3b808081, v198
	v_rcp_f32_e32 v15, v15
	v_cvt_pk_u8_f32 v14, v16, 1, v14
	v_fmamk_f32 v16, v97, 0xbfb8aa3b, v1
	v_exp_f32_e32 v16, v16
	v_cvt_pk_u8_f32 v15, v15, 0, 0
	v_fmamk_f32 v16, v16, 0x3b808081, v198
	v_rcp_f32_e32 v16, v16
	s_nop 0
	v_cvt_pk_u8_f32 v15, v16, 1, v15
	v_fmamk_f32 v16, v110, 0xbfb8aa3b, v4
	v_exp_f32_e32 v16, v16
	s_nop 0
	v_fmamk_f32 v16, v16, 0x3b808081, v198
	v_rcp_f32_e32 v16, v16
	s_nop 0
	v_cvt_pk_u8_f32 v6, v16, 2, v6
	v_fmamk_f32 v16, v106, 0xbfb8aa3b, v5
	v_exp_f32_e32 v16, v16
	s_nop 0
	v_fmamk_f32 v16, v16, 0x3b808081, v198
	v_rcp_f32_e32 v16, v16
	s_nop 0
	v_cvt_pk_u8_f32 v7, v16, 2, v7
	v_fmamk_f32 v16, v102, 0xbfb8aa3b, v4
	v_exp_f32_e32 v16, v16
	s_nop 0
	v_fmamk_f32 v16, v16, 0x3b808081, v198
	v_rcp_f32_e32 v16, v16
	s_nop 0
	v_cvt_pk_u8_f32 v14, v16, 2, v14
	v_fmamk_f32 v16, v98, 0xbfb8aa3b, v5
	v_exp_f32_e32 v16, v16
	s_nop 0
	v_fmamk_f32 v16, v16, 0x3b808081, v198
	v_rcp_f32_e32 v16, v16
	s_nop 0
	v_cvt_pk_u8_f32 v15, v16, 2, v15
	v_fmamk_f32 v16, v111, 0xbfb8aa3b, v2
	v_exp_f32_e32 v16, v16
	s_nop 0
	v_fmamk_f32 v16, v16, 0x3b808081, v198
	v_rcp_f32_e32 v16, v16
	s_nop 0
	v_cvt_pk_u8_f32 v6, v16, 3, v6
	v_fmamk_f32 v16, v107, 0xbfb8aa3b, v3
	v_exp_f32_e32 v16, v16
	s_nop 0
	v_fmamk_f32 v16, v16, 0x3b808081, v198
	v_rcp_f32_e32 v16, v16
	s_nop 0
	v_cvt_pk_u8_f32 v7, v16, 3, v7
	v_fmamk_f32 v16, v103, 0xbfb8aa3b, v2
	v_exp_f32_e32 v16, v16
	s_nop 0
	v_fmamk_f32 v16, v16, 0x3b808081, v198
	v_rcp_f32_e32 v16, v16
	s_nop 0
	v_cvt_pk_u8_f32 v16, v16, 3, v14
	v_fmamk_f32 v14, v99, 0xbfb8aa3b, v3
	v_exp_f32_e32 v14, v14
	v_or_b32_e32 v16, 0x1010101, v16
	v_fmamk_f32 v14, v14, 0x3b808081, v198
	v_rcp_f32_e32 v14, v14
	s_nop 0
	v_cvt_pk_u8_f32 v17, v14, 3, v15
	v_or_b32_e32 v14, 0x1010101, v6
	v_add_co_u32_e32 v6, vcc, s28, v8
	v_or_b32_e32 v15, 0x1010101, v7
	v_or_b32_e32 v17, 0x1010101, v17
	v_addc_co_u32_e32 v7, vcc, 0, v9, vcc
	global_store_dwordx4 v[6:7], v[14:17], off
	v_fmamk_f32 v6, v76, 0xbfb8aa3b, v13
	v_exp_f32_e32 v6, v6
	v_fmamk_f32 v16, v77, 0xbfb8aa3b, v0
	v_exp_f32_e32 v16, v16
	v_fmamk_f32 v7, v72, 0xbfb8aa3b, v12
	v_fmamk_f32 v6, v6, 0x3b808081, v198
	v_rcp_f32_e32 v6, v6
	v_fmamk_f32 v16, v16, 0x3b808081, v198
	v_rcp_f32_e32 v16, v16
	v_exp_f32_e32 v7, v7
	v_cvt_pk_u8_f32 v6, v6, 0, 0
	v_fmamk_f32 v14, v60, 0xbfb8aa3b, v13
	v_cvt_pk_u8_f32 v6, v16, 1, v6
	v_fmamk_f32 v16, v73, 0xbfb8aa3b, v1
	v_exp_f32_e32 v16, v16
	v_fmamk_f32 v7, v7, 0x3b808081, v198
	v_rcp_f32_e32 v7, v7
	v_exp_f32_e32 v14, v14
	v_fmamk_f32 v16, v16, 0x3b808081, v198
	v_rcp_f32_e32 v16, v16
	v_cvt_pk_u8_f32 v7, v7, 0, 0
	v_fmamk_f32 v14, v14, 0x3b808081, v198
	v_rcp_f32_e32 v14, v14
	v_cvt_pk_u8_f32 v7, v16, 1, v7
	v_fmamk_f32 v16, v61, 0xbfb8aa3b, v0
	v_exp_f32_e32 v16, v16
	v_cvt_pk_u8_f32 v14, v14, 0, 0
	v_fmamk_f32 v15, v56, 0xbfb8aa3b, v12
	v_exp_f32_e32 v15, v15
	v_fmamk_f32 v16, v16, 0x3b808081, v198
	v_rcp_f32_e32 v16, v16
	s_mov_b32 s28, 0xc000
	v_fmamk_f32 v15, v15, 0x3b808081, v198
	v_rcp_f32_e32 v15, v15
	v_cvt_pk_u8_f32 v14, v16, 1, v14
	v_fmamk_f32 v16, v57, 0xbfb8aa3b, v1
	v_exp_f32_e32 v16, v16
	v_cvt_pk_u8_f32 v15, v15, 0, 0
	v_fmamk_f32 v16, v16, 0x3b808081, v198
	v_rcp_f32_e32 v16, v16
	s_nop 0
	v_cvt_pk_u8_f32 v15, v16, 1, v15
	v_fmamk_f32 v16, v78, 0xbfb8aa3b, v4
	v_exp_f32_e32 v16, v16
	s_nop 0
	v_fmamk_f32 v16, v16, 0x3b808081, v198
	v_rcp_f32_e32 v16, v16
	s_nop 0
	v_cvt_pk_u8_f32 v6, v16, 2, v6
	v_fmamk_f32 v16, v74, 0xbfb8aa3b, v5
	v_exp_f32_e32 v16, v16
	s_nop 0
	v_fmamk_f32 v16, v16, 0x3b808081, v198
	v_rcp_f32_e32 v16, v16
	s_nop 0
	v_cvt_pk_u8_f32 v7, v16, 2, v7
	v_fmamk_f32 v16, v62, 0xbfb8aa3b, v4
	v_exp_f32_e32 v16, v16
	s_nop 0
	v_fmamk_f32 v16, v16, 0x3b808081, v198
	v_rcp_f32_e32 v16, v16
	s_nop 0
	v_cvt_pk_u8_f32 v14, v16, 2, v14
	v_fmamk_f32 v16, v58, 0xbfb8aa3b, v5
	v_exp_f32_e32 v16, v16
	s_nop 0
	v_fmamk_f32 v16, v16, 0x3b808081, v198
	v_rcp_f32_e32 v16, v16
	s_nop 0
	v_cvt_pk_u8_f32 v15, v16, 2, v15
	v_fmamk_f32 v16, v79, 0xbfb8aa3b, v2
	v_exp_f32_e32 v16, v16
	s_nop 0
	v_fmamk_f32 v16, v16, 0x3b808081, v198
	v_rcp_f32_e32 v16, v16
	s_nop 0
	v_cvt_pk_u8_f32 v6, v16, 3, v6
	v_fmamk_f32 v16, v75, 0xbfb8aa3b, v3
	v_exp_f32_e32 v16, v16
	s_nop 0
	v_fmamk_f32 v16, v16, 0x3b808081, v198
	v_rcp_f32_e32 v16, v16
	s_nop 0
	v_cvt_pk_u8_f32 v7, v16, 3, v7
	v_fmamk_f32 v16, v63, 0xbfb8aa3b, v2
	v_exp_f32_e32 v16, v16
	s_nop 0
	v_fmamk_f32 v16, v16, 0x3b808081, v198
	v_rcp_f32_e32 v16, v16
	s_nop 0
	v_cvt_pk_u8_f32 v16, v16, 3, v14
	v_fmamk_f32 v14, v59, 0xbfb8aa3b, v3
	v_exp_f32_e32 v14, v14
	v_or_b32_e32 v16, 0x1010101, v16
	v_fmamk_f32 v14, v14, 0x3b808081, v198
	v_rcp_f32_e32 v14, v14
	s_nop 0
	v_cvt_pk_u8_f32 v17, v14, 3, v15
	v_or_b32_e32 v14, 0x1010101, v6
	v_add_co_u32_e32 v6, vcc, s28, v8
	v_or_b32_e32 v15, 0x1010101, v7
	v_or_b32_e32 v17, 0x1010101, v17
	v_addc_co_u32_e32 v7, vcc, 0, v9, vcc
	global_store_dwordx4 v[6:7], v[14:17], off
	v_fmamk_f32 v6, v44, 0xbfb8aa3b, v13
	v_exp_f32_e32 v6, v6
	v_fmamk_f32 v14, v45, 0xbfb8aa3b, v0
	v_exp_f32_e32 v14, v14
	v_fmamk_f32 v7, v40, 0xbfb8aa3b, v12
	v_fmamk_f32 v6, v6, 0x3b808081, v198
	v_rcp_f32_e32 v6, v6
	v_fmamk_f32 v14, v14, 0x3b808081, v198
	v_rcp_f32_e32 v14, v14
	v_fmac_f32_e32 v12, 0xbfb8aa3b, v32
	v_cvt_pk_u8_f32 v6, v6, 0, 0
	v_exp_f32_e32 v12, v12
	v_cvt_pk_u8_f32 v6, v14, 1, v6
	v_fmamk_f32 v14, v41, 0xbfb8aa3b, v1
	v_fmac_f32_e32 v1, 0xbfb8aa3b, v33
	v_exp_f32_e32 v1, v1
	v_fmamk_f32 v12, v12, 0x3b808081, v198
	v_rcp_f32_e32 v12, v12
	v_fmac_f32_e32 v13, 0xbfb8aa3b, v36
	v_fmamk_f32 v1, v1, 0x3b808081, v198
	v_rcp_f32_e32 v1, v1
	v_cvt_pk_u8_f32 v12, v12, 0, 0
	v_exp_f32_e32 v13, v13
	v_fmac_f32_e32 v0, 0xbfb8aa3b, v37
	v_cvt_pk_u8_f32 v1, v1, 1, v12
	v_fmamk_f32 v12, v46, 0xbfb8aa3b, v4
	v_exp_f32_e32 v0, v0
	v_exp_f32_e32 v12, v12
	v_fmac_f32_e32 v4, 0xbfb8aa3b, v38
	v_exp_f32_e32 v4, v4
	v_fmamk_f32 v13, v13, 0x3b808081, v198
	v_rcp_f32_e32 v13, v13
	v_fmamk_f32 v0, v0, 0x3b808081, v198
	v_fmamk_f32 v12, v12, 0x3b808081, v198
	v_rcp_f32_e32 v0, v0
	v_rcp_f32_e32 v12, v12
	v_fmamk_f32 v4, v4, 0x3b808081, v198
	v_rcp_f32_e32 v4, v4
	v_cvt_pk_u8_f32 v13, v13, 0, 0
	v_cvt_pk_u8_f32 v0, v0, 1, v13
	v_cvt_pk_u8_f32 v6, v12, 2, v6
	v_fmamk_f32 v12, v42, 0xbfb8aa3b, v5
	v_fmac_f32_e32 v5, 0xbfb8aa3b, v34
	v_cvt_pk_u8_f32 v0, v4, 2, v0
	v_exp_f32_e32 v4, v5
	v_exp_f32_e32 v7, v7
	v_exp_f32_e32 v14, v14
	v_exp_f32_e32 v12, v12
	v_fmamk_f32 v4, v4, 0x3b808081, v198
	v_rcp_f32_e32 v4, v4
	v_fmamk_f32 v5, v43, 0xbfb8aa3b, v3
	v_fmac_f32_e32 v3, 0xbfb8aa3b, v35
	v_exp_f32_e32 v5, v5
	v_cvt_pk_u8_f32 v1, v4, 2, v1
	v_fmamk_f32 v4, v47, 0xbfb8aa3b, v2
	v_fmac_f32_e32 v2, 0xbfb8aa3b, v39
	v_exp_f32_e32 v2, v2
	v_exp_f32_e32 v4, v4
	v_fmamk_f32 v7, v7, 0x3b808081, v198
	v_rcp_f32_e32 v7, v7
	v_fmamk_f32 v2, v2, 0x3b808081, v198
	v_rcp_f32_e32 v2, v2
	v_fmamk_f32 v14, v14, 0x3b808081, v198
	v_rcp_f32_e32 v14, v14
	v_fmamk_f32 v12, v12, 0x3b808081, v198
	v_cvt_pk_u8_f32 v2, v2, 3, v0
	v_exp_f32_e32 v0, v3
	v_fmamk_f32 v4, v4, 0x3b808081, v198
	v_rcp_f32_e32 v12, v12
	v_rcp_f32_e32 v4, v4
	v_fmamk_f32 v5, v5, 0x3b808081, v198
	v_fmamk_f32 v0, v0, 0x3b808081, v198
	v_rcp_f32_e32 v5, v5
	v_rcp_f32_e32 v0, v0
	v_cvt_pk_u8_f32 v7, v7, 0, 0
	v_cvt_pk_u8_f32 v7, v14, 1, v7
	v_cvt_pk_u8_f32 v7, v12, 2, v7
	v_cvt_pk_u8_f32 v4, v4, 3, v6
	v_cvt_pk_u8_f32 v5, v5, 3, v7
	v_cvt_pk_u8_f32 v3, v0, 3, v1
	v_or_b32_e32 v0, 0x1010101, v4
	v_add_co_u32_e32 v4, vcc, 0xe000, v8
	v_or_b32_e32 v1, 0x1010101, v5
	v_or_b32_e32 v2, 0x1010101, v2
	v_or_b32_e32 v3, 0x1010101, v3
	v_addc_co_u32_e32 v5, vcc, 0, v9, vcc
	global_store_dwordx4 v[4:5], v[0:3], off

.LBB0_1094:
	v_mov_b32_e32 v18, v188
	s_lshl_b32 s31, s36, 7
	v_readfirstlane_b32 s30, v18
	s_lshr_b32 s36, s30, 1
	s_and_b32 s36, s36, 0x60
	s_or_b32 s31, s36, s31
	v_lshrrev_b32_e32 v0, 1, v18
	v_ashrrev_i32_e32 v167, 31, v166
	v_and_or_b32 v16, v0, 24, s31
	v_lshlrev_b64 v[0:1], 13, v[166:167]
	v_lshl_add_u64 v[0:1], s[28:29], 0, v[0:1]
	v_ashrrev_i32_e32 v17, 31, v16
	v_lshl_add_u64 v[8:9], v[16:17], 2, v[0:1]
	global_load_dwordx4 v[0:3], v[8:9], off offset:16
	global_load_dwordx4 v[4:7], v[8:9], off
	s_movk_i32 s31, 0x1000
	v_lshl_add_u64 v[10:11], v[8:9], 0, s[84:85]
	v_add_co_u32_e32 v8, vcc, s31, v8
	s_ashr_i32 s30, s30, 2
	s_nop 0
	v_addc_co_u32_e32 v9, vcc, 0, v9, vcc
	global_load_dwordx4 v[12:15], v[8:9], off
	s_nop 0
	global_load_dwordx4 v[8:11], v[10:11], off offset:16
	v_lshlrev_b32_e32 v19, 8, v219
	s_andn2_b32 s30, s30, 63
	v_add_u32_e32 v19, s30, v19
	v_and_or_b32 v18, v18, 15, v19
	v_ashrrev_i32_e32 v19, 31, v18
	v_readlane_b32 s30, v254, 30
	v_lshlrev_b64 v[18:19], 10, v[18:19]
	v_readlane_b32 s31, v254, 31
	s_mov_b32 s21, 0x24000
	s_mov_b64 s[40:41], -1
	v_lshl_add_u64 v[18:19], s[30:31], 0, v[18:19]
	v_lshl_add_u64 v[16:17], v[18:19], 0, v[16:17]
	s_mov_b32 s30, 0xc000
	s_mov_b64 s[72:73], 0x400
	v_readlane_b32 s70, v255, 14
	s_mov_b32 s71, s66
	s_waitcnt vmcnt(0)
	v_add_f32_e32 v18, v158, v4
	v_min_f32_e32 v18, 0x40e00000, v18
	v_mul_f32_e32 v20, 0x3fd9db23, v18
	v_mul_f32_e32 v20, 0xbfb8aa3b, v20
	v_exp_f32_e32 v20, v20
	v_add_f32_e32 v12, 1.0, v12
	v_add_f32_e32 v20, 1.0, v20
	v_rcp_f32_e32 v20, v20
	v_add_f32_e32 v19, v154, v12
	v_med3_f32 v19, v19, s61, v214
	v_add_f32_e32 v8, 1.0, v8
	v_mul_f32_e32 v18, v18, v20
	v_mul_f32_e32 v18, v19, v18
	v_add_f32_e32 v19, v150, v0
	v_min_f32_e32 v19, 0x40e00000, v19
	v_mul_f32_e32 v21, 0x3fd9db23, v19
	v_mul_f32_e32 v21, 0xbfb8aa3b, v21
	v_exp_f32_e32 v21, v21
	v_add_f32_e32 v20, v146, v8
	v_med3_f32 v20, v20, s61, v214
	v_add_f32_e32 v13, 1.0, v13
	v_add_f32_e32 v21, 1.0, v21
	v_rcp_f32_e32 v21, v21
	v_add_f32_e32 v9, 1.0, v9
	v_add_f32_e32 v14, 1.0, v14
	v_add_f32_e32 v10, 1.0, v10
	v_mul_f32_e32 v19, v19, v21
	v_mul_f32_e32 v19, v20, v19
	v_add_f32_e32 v20, v159, v5
	v_min_f32_e32 v20, 0x40e00000, v20
	v_mul_f32_e32 v22, 0x3fd9db23, v20
	v_mul_f32_e32 v22, 0xbfb8aa3b, v22
	v_exp_f32_e32 v22, v22
	v_add_f32_e32 v21, v155, v13
	v_med3_f32 v21, v21, s61, v214
	v_add_f32_e32 v15, 1.0, v15
	v_add_f32_e32 v22, 1.0, v22
	v_rcp_f32_e32 v22, v22
	v_add_f32_e32 v11, 1.0, v11
	v_mul_f32_e32 v20, v20, v22
	v_mul_f32_e32 v20, v21, v20
	v_add_f32_e32 v21, v151, v1
	v_min_f32_e32 v21, 0x40e00000, v21
	v_mul_f32_e32 v23, 0x3fd9db23, v21
	v_mul_f32_e32 v23, 0xbfb8aa3b, v23
	v_exp_f32_e32 v23, v23
	v_add_f32_e32 v22, v147, v9
	v_med3_f32 v22, v22, s61, v214
	v_add_f32_e32 v23, 1.0, v23
	v_rcp_f32_e32 v23, v23
	s_nop 0
	v_mul_f32_e32 v21, v21, v23
	v_mul_f32_e32 v21, v22, v21
	v_add_f32_e32 v22, v160, v6
	v_min_f32_e32 v22, 0x40e00000, v22
	v_mul_f32_e32 v24, 0x3fd9db23, v22
	v_mul_f32_e32 v24, 0xbfb8aa3b, v24
	v_exp_f32_e32 v24, v24
	v_add_f32_e32 v23, v156, v14
	v_med3_f32 v23, v23, s61, v214
	v_add_f32_e32 v24, 1.0, v24
	v_rcp_f32_e32 v24, v24
	s_nop 0
	v_mul_f32_e32 v22, v22, v24
	v_mul_f32_e32 v23, v23, v22
	v_add_f32_e32 v22, v152, v2
	v_min_f32_e32 v22, 0x40e00000, v22
	v_mul_f32_e32 v25, 0x3fd9db23, v22
	v_mul_f32_e32 v25, 0xbfb8aa3b, v25
	v_exp_f32_e32 v25, v25
	v_add_f32_e32 v24, v148, v10
	v_med3_f32 v24, v24, s61, v214
	v_add_f32_e32 v25, 1.0, v25
	v_rcp_f32_e32 v25, v25
	s_nop 0
	v_mul_f32_e32 v22, v22, v25
	v_mul_f32_e32 v24, v24, v22
	v_add_f32_e32 v22, v161, v7
	v_min_f32_e32 v22, 0x40e00000, v22
	v_mul_f32_e32 v26, 0x3fd9db23, v22
	v_mul_f32_e32 v26, 0xbfb8aa3b, v26
	v_exp_f32_e32 v26, v26
	v_add_f32_e32 v25, v157, v15
	v_med3_f32 v25, v25, s61, v214
	v_add_f32_e32 v26, 1.0, v26
	v_rcp_f32_e32 v26, v26
	s_nop 0
	v_mul_f32_e32 v22, v22, v26
	v_mul_f32_e32 v25, v25, v22
	v_add_f32_e32 v22, v153, v3
	v_min_f32_e32 v22, 0x40e00000, v22
	v_mul_f32_e32 v27, 0x3fd9db23, v22
	v_mul_f32_e32 v27, 0xbfb8aa3b, v27
	v_exp_f32_e32 v27, v27
	v_add_f32_e32 v26, v149, v11
	v_med3_f32 v26, v26, s61, v214
	v_add_f32_e32 v27, 1.0, v27
	v_rcp_f32_e32 v27, v27
	s_nop 0
	v_mul_f32_e32 v22, v22, v27
	v_mul_f32_e32 v26, v26, v22
	v_mov_b32_e32 v22, v113
	v_cvt_pk_fp8_f32 v22, v18, v20
	v_add_f32_e32 v18, v142, v4
	v_min_f32_e32 v18, 0x40e00000, v18
	v_mul_f32_e32 v20, 0x3fd9db23, v18
	v_mul_f32_e32 v20, 0xbfb8aa3b, v20
	v_exp_f32_e32 v20, v20
	v_cvt_pk_fp8_f32 v22, v23, v25 op_sel:[0,0,1]
	v_mov_b32_e32 v23, v113
	v_cvt_pk_fp8_f32 v23, v19, v21
	v_add_f32_e32 v20, 1.0, v20
	v_rcp_f32_e32 v20, v20
	v_add_f32_e32 v19, v138, v12
	v_med3_f32 v19, v19, s61, v214
	v_cvt_pk_fp8_f32 v23, v24, v26 op_sel:[0,0,1]
	v_mul_f32_e32 v18, v18, v20
	v_mul_f32_e32 v19, v19, v18
	v_add_f32_e32 v18, v134, v0
	v_min_f32_e32 v18, 0x40e00000, v18
	v_mul_f32_e32 v21, 0x3fd9db23, v18
	v_mul_f32_e32 v21, 0xbfb8aa3b, v21
	v_exp_f32_e32 v21, v21
	v_add_f32_e32 v20, v130, v8
	v_med3_f32 v20, v20, s61, v214
	global_store_dwordx2 v[16:17], v[22:23], off
	v_add_f32_e32 v21, 1.0, v21
	v_rcp_f32_e32 v21, v21
	s_nop 0
	v_mul_f32_e32 v18, v18, v21
	v_mul_f32_e32 v20, v20, v18
	v_add_f32_e32 v18, v143, v5
	v_min_f32_e32 v18, 0x40e00000, v18
	v_mul_f32_e32 v22, 0x3fd9db23, v18
	v_mul_f32_e32 v22, 0xbfb8aa3b, v22
	v_exp_f32_e32 v22, v22
	v_add_f32_e32 v21, v139, v13
	v_med3_f32 v21, v21, s61, v214
	v_add_f32_e32 v22, 1.0, v22
	v_rcp_f32_e32 v22, v22
	s_nop 0
	v_mul_f32_e32 v18, v18, v22
	v_mul_f32_e32 v21, v21, v18
	v_add_f32_e32 v18, v135, v1
	v_min_f32_e32 v18, 0x40e00000, v18
	v_mul_f32_e32 v23, 0x3fd9db23, v18
	v_mul_f32_e32 v23, 0xbfb8aa3b, v23
	v_exp_f32_e32 v23, v23
	v_add_f32_e32 v22, v131, v9
	v_med3_f32 v22, v22, s61, v214
	v_add_f32_e32 v23, 1.0, v23
	v_rcp_f32_e32 v23, v23
	s_nop 0
	v_mul_f32_e32 v18, v18, v23
	v_mul_f32_e32 v22, v22, v18
	v_add_f32_e32 v18, v144, v6
	v_min_f32_e32 v18, 0x40e00000, v18
	v_mul_f32_e32 v24, 0x3fd9db23, v18
	v_mul_f32_e32 v24, 0xbfb8aa3b, v24
	v_exp_f32_e32 v24, v24
	v_add_f32_e32 v23, v140, v14
	v_med3_f32 v23, v23, s61, v214
	v_add_f32_e32 v24, 1.0, v24
	v_rcp_f32_e32 v24, v24
	s_nop 0
	v_mul_f32_e32 v18, v18, v24
	v_mul_f32_e32 v23, v23, v18
	v_add_f32_e32 v18, v136, v2
	v_min_f32_e32 v18, 0x40e00000, v18
	v_mul_f32_e32 v25, 0x3fd9db23, v18
	v_mul_f32_e32 v25, 0xbfb8aa3b, v25
	v_exp_f32_e32 v25, v25
	v_add_f32_e32 v24, v132, v10
	v_med3_f32 v24, v24, s61, v214
	v_add_f32_e32 v25, 1.0, v25
	v_rcp_f32_e32 v25, v25
	s_nop 0
	v_mul_f32_e32 v18, v18, v25
	v_mul_f32_e32 v24, v24, v18
	v_add_f32_e32 v18, v145, v7
	v_min_f32_e32 v18, 0x40e00000, v18
	v_mul_f32_e32 v26, 0x3fd9db23, v18
	v_mul_f32_e32 v26, 0xbfb8aa3b, v26
	v_exp_f32_e32 v26, v26
	v_add_f32_e32 v25, v141, v15
	v_med3_f32 v25, v25, s61, v214
	v_add_f32_e32 v26, 1.0, v26
	v_rcp_f32_e32 v26, v26
	s_nop 0
	v_mul_f32_e32 v18, v18, v26
	v_mul_f32_e32 v25, v25, v18
	v_add_f32_e32 v18, v137, v3
	v_min_f32_e32 v18, 0x40e00000, v18
	v_mul_f32_e32 v27, 0x3fd9db23, v18
	v_mul_f32_e32 v27, 0xbfb8aa3b, v27
	v_exp_f32_e32 v27, v27
	v_add_f32_e32 v26, v133, v11
	v_med3_f32 v26, v26, s61, v214
	v_add_f32_e32 v27, 1.0, v27
	v_rcp_f32_e32 v27, v27
	s_nop 0
	v_mul_f32_e32 v18, v18, v27
	v_mul_f32_e32 v26, v26, v18
	v_mov_b32_e32 v18, v113
	v_cvt_pk_fp8_f32 v18, v19, v21
	v_mov_b32_e32 v19, v113
	v_cvt_pk_fp8_f32 v19, v20, v22
	v_add_co_u32_e32 v20, vcc, s62, v16
	v_cvt_pk_fp8_f32 v18, v23, v25 op_sel:[0,0,1]
	v_cvt_pk_fp8_f32 v19, v24, v26 op_sel:[0,0,1]
	v_addc_co_u32_e32 v21, vcc, 0, v17, vcc
	global_store_dwordx2 v[20:21], v[18:19], off
	v_add_f32_e32 v18, v126, v4
	v_min_f32_e32 v18, 0x40e00000, v18
	v_mul_f32_e32 v20, 0x3fd9db23, v18
	v_mul_f32_e32 v20, 0xbfb8aa3b, v20
	v_exp_f32_e32 v20, v20
	v_add_f32_e32 v19, v122, v12
	v_med3_f32 v19, v19, s61, v214
	v_add_f32_e32 v20, 1.0, v20
	v_rcp_f32_e32 v20, v20
	s_nop 0
	v_mul_f32_e32 v18, v18, v20
	v_mul_f32_e32 v19, v19, v18
	v_add_f32_e32 v18, v118, v0
	v_min_f32_e32 v18, 0x40e00000, v18
	v_mul_f32_e32 v21, 0x3fd9db23, v18
	v_mul_f32_e32 v21, 0xbfb8aa3b, v21
	v_exp_f32_e32 v21, v21
	v_add_f32_e32 v20, v114, v8
	v_med3_f32 v20, v20, s61, v214
	v_add_f32_e32 v21, 1.0, v21
	v_rcp_f32_e32 v21, v21
	s_nop 0
	v_mul_f32_e32 v18, v18, v21
	v_mul_f32_e32 v20, v20, v18
	v_add_f32_e32 v18, v127, v5
	v_min_f32_e32 v18, 0x40e00000, v18
	v_mul_f32_e32 v22, 0x3fd9db23, v18
	v_mul_f32_e32 v22, 0xbfb8aa3b, v22
	v_exp_f32_e32 v22, v22
	v_add_f32_e32 v21, v123, v13
	v_med3_f32 v21, v21, s61, v214
	v_add_f32_e32 v22, 1.0, v22
	v_rcp_f32_e32 v22, v22
	s_nop 0
	v_mul_f32_e32 v18, v18, v22
	v_mul_f32_e32 v21, v21, v18
	v_add_f32_e32 v18, v119, v1
	v_min_f32_e32 v18, 0x40e00000, v18
	v_mul_f32_e32 v23, 0x3fd9db23, v18
	v_mul_f32_e32 v23, 0xbfb8aa3b, v23
	v_exp_f32_e32 v23, v23
	v_add_f32_e32 v22, v115, v9
	v_med3_f32 v22, v22, s61, v214
	v_add_f32_e32 v23, 1.0, v23
	v_rcp_f32_e32 v23, v23
	s_nop 0
	v_mul_f32_e32 v18, v18, v23
	v_mul_f32_e32 v22, v22, v18
	v_add_f32_e32 v18, v128, v6
	v_min_f32_e32 v18, 0x40e00000, v18
	v_mul_f32_e32 v24, 0x3fd9db23, v18
	v_mul_f32_e32 v24, 0xbfb8aa3b, v24
	v_exp_f32_e32 v24, v24
	v_add_f32_e32 v23, v124, v14
	v_med3_f32 v23, v23, s61, v214
	v_add_f32_e32 v24, 1.0, v24
	v_rcp_f32_e32 v24, v24
	s_nop 0
	v_mul_f32_e32 v18, v18, v24
	v_mul_f32_e32 v23, v23, v18
	v_add_f32_e32 v18, v120, v2
	v_min_f32_e32 v18, 0x40e00000, v18
	v_mul_f32_e32 v25, 0x3fd9db23, v18
	v_mul_f32_e32 v25, 0xbfb8aa3b, v25
	v_exp_f32_e32 v25, v25
	v_add_f32_e32 v24, v116, v10
	v_med3_f32 v24, v24, s61, v214
	v_add_f32_e32 v25, 1.0, v25
	v_rcp_f32_e32 v25, v25
	s_nop 0
	v_mul_f32_e32 v18, v18, v25
	v_mul_f32_e32 v24, v24, v18
	v_add_f32_e32 v18, v129, v7
	v_min_f32_e32 v18, 0x40e00000, v18
	v_mul_f32_e32 v26, 0x3fd9db23, v18
	v_mul_f32_e32 v26, 0xbfb8aa3b, v26
	v_exp_f32_e32 v26, v26
	v_add_f32_e32 v25, v125, v15
	v_med3_f32 v25, v25, s61, v214
	v_add_f32_e32 v26, 1.0, v26
	v_rcp_f32_e32 v26, v26
	s_nop 0
	v_mul_f32_e32 v18, v18, v26
	v_mul_f32_e32 v25, v25, v18
	v_add_f32_e32 v18, v121, v3
	v_min_f32_e32 v18, 0x40e00000, v18
	v_mul_f32_e32 v27, 0x3fd9db23, v18
	v_mul_f32_e32 v27, 0xbfb8aa3b, v27
	v_exp_f32_e32 v27, v27
	v_add_f32_e32 v26, v117, v11
	v_med3_f32 v26, v26, s61, v214
	v_add_f32_e32 v27, 1.0, v27
	v_rcp_f32_e32 v27, v27
	s_nop 0
	v_mul_f32_e32 v18, v18, v27
	v_mul_f32_e32 v26, v26, v18
	v_mov_b32_e32 v18, v113
	v_cvt_pk_fp8_f32 v18, v19, v21
	v_mov_b32_e32 v19, v113
	v_cvt_pk_fp8_f32 v19, v20, v22
	v_add_co_u32_e32 v20, vcc, s24, v16
	v_cvt_pk_fp8_f32 v18, v23, v25 op_sel:[0,0,1]
	v_cvt_pk_fp8_f32 v19, v24, v26 op_sel:[0,0,1]
	v_addc_co_u32_e32 v21, vcc, 0, v17, vcc
	global_store_dwordx2 v[20:21], v[18:19], off
	v_add_f32_e32 v18, v108, v4
	v_min_f32_e32 v18, 0x40e00000, v18
	v_mul_f32_e32 v20, 0x3fd9db23, v18
	v_mul_f32_e32 v20, 0xbfb8aa3b, v20
	v_exp_f32_e32 v20, v20
	v_add_f32_e32 v19, v104, v12
	v_med3_f32 v19, v19, s61, v214
	v_add_f32_e32 v20, 1.0, v20
	v_rcp_f32_e32 v20, v20
	s_nop 0
	v_mul_f32_e32 v18, v18, v20
	v_mul_f32_e32 v19, v19, v18
	v_add_f32_e32 v18, v100, v0
	v_min_f32_e32 v18, 0x40e00000, v18
	v_mul_f32_e32 v21, 0x3fd9db23, v18
	v_mul_f32_e32 v21, 0xbfb8aa3b, v21
	v_exp_f32_e32 v21, v21
	v_add_f32_e32 v20, v96, v8
	v_med3_f32 v20, v20, s61, v214
	v_add_f32_e32 v21, 1.0, v21
	v_rcp_f32_e32 v21, v21
	s_nop 0
	v_mul_f32_e32 v18, v18, v21
	v_mul_f32_e32 v20, v20, v18
	v_add_f32_e32 v18, v109, v5
	v_min_f32_e32 v18, 0x40e00000, v18
	v_mul_f32_e32 v22, 0x3fd9db23, v18
	v_mul_f32_e32 v22, 0xbfb8aa3b, v22
	v_exp_f32_e32 v22, v22
	v_add_f32_e32 v21, v105, v13
	v_med3_f32 v21, v21, s61, v214
	v_add_f32_e32 v22, 1.0, v22
	v_rcp_f32_e32 v22, v22
	s_nop 0
	v_mul_f32_e32 v18, v18, v22
	v_mul_f32_e32 v21, v21, v18
	v_add_f32_e32 v18, v101, v1
	v_min_f32_e32 v18, 0x40e00000, v18
	v_mul_f32_e32 v23, 0x3fd9db23, v18
	v_mul_f32_e32 v23, 0xbfb8aa3b, v23
	v_exp_f32_e32 v23, v23
	v_add_f32_e32 v22, v97, v9
	v_med3_f32 v22, v22, s61, v214
	v_add_f32_e32 v23, 1.0, v23
	v_rcp_f32_e32 v23, v23
	s_nop 0
	v_mul_f32_e32 v18, v18, v23
	v_mul_f32_e32 v22, v22, v18
	v_add_f32_e32 v18, v110, v6
	v_min_f32_e32 v18, 0x40e00000, v18
	v_mul_f32_e32 v24, 0x3fd9db23, v18
	v_mul_f32_e32 v24, 0xbfb8aa3b, v24
	v_exp_f32_e32 v24, v24
	v_add_f32_e32 v23, v106, v14
	v_med3_f32 v23, v23, s61, v214
	v_add_f32_e32 v24, 1.0, v24
	v_rcp_f32_e32 v24, v24
	s_nop 0
	v_mul_f32_e32 v18, v18, v24
	v_mul_f32_e32 v23, v23, v18
	v_add_f32_e32 v18, v102, v2
	v_min_f32_e32 v18, 0x40e00000, v18
	v_mul_f32_e32 v25, 0x3fd9db23, v18
	v_mul_f32_e32 v25, 0xbfb8aa3b, v25
	v_exp_f32_e32 v25, v25
	v_add_f32_e32 v24, v98, v10
	v_med3_f32 v24, v24, s61, v214
	v_add_f32_e32 v25, 1.0, v25
	v_rcp_f32_e32 v25, v25
	s_nop 0
	v_mul_f32_e32 v18, v18, v25
	v_mul_f32_e32 v24, v24, v18
	v_add_f32_e32 v18, v111, v7
	v_min_f32_e32 v18, 0x40e00000, v18
	v_mul_f32_e32 v26, 0x3fd9db23, v18
	v_mul_f32_e32 v26, 0xbfb8aa3b, v26
	v_exp_f32_e32 v26, v26
	v_add_f32_e32 v25, v107, v15
	v_med3_f32 v25, v25, s61, v214
	v_add_f32_e32 v26, 1.0, v26
	v_rcp_f32_e32 v26, v26
	s_nop 0
	v_mul_f32_e32 v18, v18, v26
	v_mul_f32_e32 v25, v25, v18
	v_add_f32_e32 v18, v103, v3
	v_min_f32_e32 v18, 0x40e00000, v18
	v_mul_f32_e32 v27, 0x3fd9db23, v18
	v_mul_f32_e32 v27, 0xbfb8aa3b, v27
	v_exp_f32_e32 v27, v27
	v_add_f32_e32 v26, v99, v11
	v_med3_f32 v26, v26, s61, v214
	v_add_f32_e32 v27, 1.0, v27
	v_rcp_f32_e32 v27, v27
	s_nop 0
	v_mul_f32_e32 v18, v18, v27
	v_mul_f32_e32 v26, v26, v18
	v_mov_b32_e32 v18, v113
	v_cvt_pk_fp8_f32 v18, v19, v21
	v_mov_b32_e32 v19, v113
	v_cvt_pk_fp8_f32 v19, v20, v22
	v_add_co_u32_e32 v20, vcc, s30, v16
	v_cvt_pk_fp8_f32 v18, v23, v25 op_sel:[0,0,1]
	v_cvt_pk_fp8_f32 v19, v24, v26 op_sel:[0,0,1]
	v_addc_co_u32_e32 v21, vcc, 0, v17, vcc
	global_store_dwordx2 v[20:21], v[18:19], off
	v_add_f32_e32 v18, v92, v4
	v_min_f32_e32 v18, 0x40e00000, v18
	v_mul_f32_e32 v20, 0x3fd9db23, v18
	v_mul_f32_e32 v20, 0xbfb8aa3b, v20
	v_exp_f32_e32 v20, v20
	v_add_f32_e32 v19, v88, v12
	v_med3_f32 v19, v19, s61, v214
	v_add_f32_e32 v20, 1.0, v20
	v_rcp_f32_e32 v20, v20
	s_nop 0
	v_mul_f32_e32 v18, v18, v20
	v_mul_f32_e32 v19, v19, v18
	v_add_f32_e32 v18, v84, v0
	v_min_f32_e32 v18, 0x40e00000, v18
	v_mul_f32_e32 v21, 0x3fd9db23, v18
	v_mul_f32_e32 v21, 0xbfb8aa3b, v21
	v_exp_f32_e32 v21, v21
	v_add_f32_e32 v20, v80, v8
	v_med3_f32 v20, v20, s61, v214
	v_add_f32_e32 v21, 1.0, v21
	v_rcp_f32_e32 v21, v21
	s_nop 0
	v_mul_f32_e32 v18, v18, v21
	v_mul_f32_e32 v20, v20, v18
	v_add_f32_e32 v18, v93, v5
	v_min_f32_e32 v18, 0x40e00000, v18
	v_mul_f32_e32 v22, 0x3fd9db23, v18
	v_mul_f32_e32 v22, 0xbfb8aa3b, v22
	v_exp_f32_e32 v22, v22
	v_add_f32_e32 v21, v89, v13
	v_med3_f32 v21, v21, s61, v214
	v_add_f32_e32 v22, 1.0, v22
	v_rcp_f32_e32 v22, v22
	s_nop 0
	v_mul_f32_e32 v18, v18, v22
	v_mul_f32_e32 v21, v21, v18
	v_add_f32_e32 v18, v85, v1
	v_min_f32_e32 v18, 0x40e00000, v18
	v_mul_f32_e32 v23, 0x3fd9db23, v18
	v_mul_f32_e32 v23, 0xbfb8aa3b, v23
	v_exp_f32_e32 v23, v23
	v_add_f32_e32 v22, v81, v9
	v_med3_f32 v22, v22, s61, v214
	v_add_f32_e32 v23, 1.0, v23
	v_rcp_f32_e32 v23, v23
	s_nop 0
	v_mul_f32_e32 v18, v18, v23
	v_mul_f32_e32 v22, v22, v18
	v_add_f32_e32 v18, v94, v6
	v_min_f32_e32 v18, 0x40e00000, v18
	v_mul_f32_e32 v24, 0x3fd9db23, v18
	v_mul_f32_e32 v24, 0xbfb8aa3b, v24
	v_exp_f32_e32 v24, v24
	v_add_f32_e32 v23, v90, v14
	v_med3_f32 v23, v23, s61, v214
	v_add_f32_e32 v24, 1.0, v24
	v_rcp_f32_e32 v24, v24
	s_nop 0
	v_mul_f32_e32 v18, v18, v24
	v_mul_f32_e32 v23, v23, v18
	v_add_f32_e32 v18, v86, v2
	v_min_f32_e32 v18, 0x40e00000, v18
	v_mul_f32_e32 v25, 0x3fd9db23, v18
	v_mul_f32_e32 v25, 0xbfb8aa3b, v25
	v_exp_f32_e32 v25, v25
	v_add_f32_e32 v24, v82, v10
	v_med3_f32 v24, v24, s61, v214
	v_add_f32_e32 v25, 1.0, v25
	v_rcp_f32_e32 v25, v25
	s_nop 0
	v_mul_f32_e32 v18, v18, v25
	v_mul_f32_e32 v24, v24, v18
	v_add_f32_e32 v18, v95, v7
	v_min_f32_e32 v18, 0x40e00000, v18
	v_mul_f32_e32 v26, 0x3fd9db23, v18
	v_mul_f32_e32 v26, 0xbfb8aa3b, v26
	v_exp_f32_e32 v26, v26
	v_add_f32_e32 v25, v91, v15
	v_med3_f32 v25, v25, s61, v214
	v_add_f32_e32 v26, 1.0, v26
	v_rcp_f32_e32 v26, v26
	s_nop 0
	v_mul_f32_e32 v18, v18, v26
	v_mul_f32_e32 v25, v25, v18
	v_add_f32_e32 v18, v87, v3
	v_min_f32_e32 v18, 0x40e00000, v18
	v_mul_f32_e32 v27, 0x3fd9db23, v18
	v_mul_f32_e32 v27, 0xbfb8aa3b, v27
	v_exp_f32_e32 v27, v27
	v_add_f32_e32 v26, v83, v11
	v_med3_f32 v26, v26, s61, v214
	v_add_f32_e32 v27, 1.0, v27
	v_rcp_f32_e32 v27, v27
	s_nop 0
	v_mul_f32_e32 v18, v18, v27
	v_mul_f32_e32 v26, v26, v18
	v_mov_b32_e32 v18, v113
	v_cvt_pk_fp8_f32 v18, v19, v21
	v_mov_b32_e32 v19, v113
	v_cvt_pk_fp8_f32 v19, v20, v22
	v_add_co_u32_e32 v20, vcc, s63, v16
	v_cvt_pk_fp8_f32 v18, v23, v25 op_sel:[0,0,1]
	v_cvt_pk_fp8_f32 v19, v24, v26 op_sel:[0,0,1]
	v_addc_co_u32_e32 v21, vcc, 0, v17, vcc
	global_store_dwordx2 v[20:21], v[18:19], off
	v_add_f32_e32 v18, v76, v4
	v_min_f32_e32 v18, 0x40e00000, v18
	v_mul_f32_e32 v20, 0x3fd9db23, v18
	v_mul_f32_e32 v20, 0xbfb8aa3b, v20
	v_exp_f32_e32 v20, v20
	v_add_f32_e32 v19, v72, v12
	v_med3_f32 v19, v19, s61, v214
	v_add_f32_e32 v20, 1.0, v20
	v_rcp_f32_e32 v20, v20
	s_nop 0
	v_mul_f32_e32 v18, v18, v20
	v_mul_f32_e32 v19, v19, v18
	v_add_f32_e32 v18, v68, v0
	v_min_f32_e32 v18, 0x40e00000, v18
	v_mul_f32_e32 v21, 0x3fd9db23, v18
	v_mul_f32_e32 v21, 0xbfb8aa3b, v21
	v_exp_f32_e32 v21, v21
	v_add_f32_e32 v20, v64, v8
	v_med3_f32 v20, v20, s61, v214
	v_add_f32_e32 v21, 1.0, v21
	v_rcp_f32_e32 v21, v21
	s_nop 0
	v_mul_f32_e32 v18, v18, v21
	v_mul_f32_e32 v20, v20, v18
	v_add_f32_e32 v18, v77, v5
	v_min_f32_e32 v18, 0x40e00000, v18
	v_mul_f32_e32 v22, 0x3fd9db23, v18
	v_mul_f32_e32 v22, 0xbfb8aa3b, v22
	v_exp_f32_e32 v22, v22
	v_add_f32_e32 v21, v73, v13
	v_med3_f32 v21, v21, s61, v214
	v_add_f32_e32 v22, 1.0, v22
	v_rcp_f32_e32 v22, v22
	s_nop 0
	v_mul_f32_e32 v18, v18, v22
	v_mul_f32_e32 v21, v21, v18
	v_add_f32_e32 v18, v69, v1
	v_min_f32_e32 v18, 0x40e00000, v18
	v_mul_f32_e32 v23, 0x3fd9db23, v18
	v_mul_f32_e32 v23, 0xbfb8aa3b, v23
	v_exp_f32_e32 v23, v23
	v_add_f32_e32 v22, v65, v9
	v_med3_f32 v22, v22, s61, v214
	v_add_f32_e32 v23, 1.0, v23
	v_rcp_f32_e32 v23, v23
	s_nop 0
	v_mul_f32_e32 v18, v18, v23
	v_mul_f32_e32 v22, v22, v18
	v_add_f32_e32 v18, v78, v6
	v_min_f32_e32 v18, 0x40e00000, v18
	v_mul_f32_e32 v24, 0x3fd9db23, v18
	v_mul_f32_e32 v24, 0xbfb8aa3b, v24
	v_exp_f32_e32 v24, v24
	v_add_f32_e32 v23, v74, v14
	v_med3_f32 v23, v23, s61, v214
	v_add_f32_e32 v24, 1.0, v24
	v_rcp_f32_e32 v24, v24
	s_nop 0
	v_mul_f32_e32 v18, v18, v24
	v_mul_f32_e32 v23, v23, v18
	v_add_f32_e32 v18, v70, v2
	v_min_f32_e32 v18, 0x40e00000, v18
	v_mul_f32_e32 v25, 0x3fd9db23, v18
	v_mul_f32_e32 v25, 0xbfb8aa3b, v25
	v_exp_f32_e32 v25, v25
	v_add_f32_e32 v24, v66, v10
	v_med3_f32 v24, v24, s61, v214
	v_add_f32_e32 v25, 1.0, v25
	v_rcp_f32_e32 v25, v25
	s_nop 0
	v_mul_f32_e32 v18, v18, v25
	v_mul_f32_e32 v24, v24, v18
	v_add_f32_e32 v18, v79, v7
	v_min_f32_e32 v18, 0x40e00000, v18
	v_mul_f32_e32 v26, 0x3fd9db23, v18
	v_mul_f32_e32 v26, 0xbfb8aa3b, v26
	v_exp_f32_e32 v26, v26
	v_add_f32_e32 v25, v75, v15
	v_med3_f32 v25, v25, s61, v214
	v_add_f32_e32 v26, 1.0, v26
	v_rcp_f32_e32 v26, v26
	s_nop 0
	v_mul_f32_e32 v18, v18, v26
	v_mul_f32_e32 v25, v25, v18
	v_add_f32_e32 v18, v71, v3
	v_min_f32_e32 v18, 0x40e00000, v18
	v_mul_f32_e32 v27, 0x3fd9db23, v18
	v_mul_f32_e32 v27, 0xbfb8aa3b, v27
	v_exp_f32_e32 v27, v27
	v_add_f32_e32 v26, v67, v11
	v_med3_f32 v26, v26, s61, v214
	v_add_f32_e32 v27, 1.0, v27
	v_rcp_f32_e32 v27, v27
	s_nop 0
	v_mul_f32_e32 v18, v18, v27
	v_mul_f32_e32 v26, v26, v18
	v_mov_b32_e32 v18, v113
	v_cvt_pk_fp8_f32 v18, v19, v21
	v_mov_b32_e32 v19, v113
	v_cvt_pk_fp8_f32 v19, v20, v22
	v_add_co_u32_e32 v20, vcc, s21, v16
	v_cvt_pk_fp8_f32 v18, v23, v25 op_sel:[0,0,1]
	v_cvt_pk_fp8_f32 v19, v24, v26 op_sel:[0,0,1]
	v_addc_co_u32_e32 v21, vcc, 0, v17, vcc
	s_mov_b32 s21, 0x28000
	global_store_dwordx2 v[20:21], v[18:19], off
	v_add_f32_e32 v18, v60, v4
	v_min_f32_e32 v18, 0x40e00000, v18
	v_mul_f32_e32 v20, 0x3fd9db23, v18
	v_mul_f32_e32 v20, 0xbfb8aa3b, v20
	v_exp_f32_e32 v20, v20
	v_add_f32_e32 v19, v56, v12
	v_med3_f32 v19, v19, s61, v214
	v_add_f32_e32 v4, v44, v4
	v_add_f32_e32 v20, 1.0, v20
	v_rcp_f32_e32 v20, v20
	v_min_f32_e32 v4, 0x40e00000, v4
	v_add_f32_e32 v12, v40, v12
	v_med3_f32 v12, v12, s61, v214
	v_mul_f32_e32 v18, v18, v20
	v_mul_f32_e32 v19, v19, v18
	v_add_f32_e32 v18, v52, v0
	v_min_f32_e32 v18, 0x40e00000, v18
	v_mul_f32_e32 v21, 0x3fd9db23, v18
	v_mul_f32_e32 v21, 0xbfb8aa3b, v21
	v_exp_f32_e32 v21, v21
	v_add_f32_e32 v20, v48, v8
	v_med3_f32 v20, v20, s61, v214
	v_add_f32_e32 v0, v36, v0
	v_add_f32_e32 v21, 1.0, v21
	v_rcp_f32_e32 v21, v21
	v_min_f32_e32 v0, 0x40e00000, v0
	v_add_f32_e32 v8, v32, v8
	v_med3_f32 v8, v8, s61, v214
	v_mul_f32_e32 v18, v18, v21
	v_mul_f32_e32 v20, v20, v18
	v_add_f32_e32 v18, v61, v5
	v_min_f32_e32 v18, 0x40e00000, v18
	v_mul_f32_e32 v22, 0x3fd9db23, v18
	v_mul_f32_e32 v22, 0xbfb8aa3b, v22
	v_exp_f32_e32 v22, v22
	v_add_f32_e32 v21, v57, v13
	v_med3_f32 v21, v21, s61, v214
	v_add_f32_e32 v22, 1.0, v22
	v_rcp_f32_e32 v22, v22
	s_nop 0
	v_mul_f32_e32 v18, v18, v22
	v_mul_f32_e32 v21, v21, v18
	v_add_f32_e32 v18, v53, v1
	v_min_f32_e32 v18, 0x40e00000, v18
	v_mul_f32_e32 v23, 0x3fd9db23, v18
	v_mul_f32_e32 v23, 0xbfb8aa3b, v23
	v_exp_f32_e32 v23, v23
	v_add_f32_e32 v22, v49, v9
	v_med3_f32 v22, v22, s61, v214
	v_add_f32_e32 v23, 1.0, v23
	v_rcp_f32_e32 v23, v23
	s_nop 0
	v_mul_f32_e32 v18, v18, v23
	v_mul_f32_e32 v22, v22, v18
	v_add_f32_e32 v18, v62, v6
	v_min_f32_e32 v18, 0x40e00000, v18
	v_mul_f32_e32 v24, 0x3fd9db23, v18
	v_mul_f32_e32 v24, 0xbfb8aa3b, v24
	v_exp_f32_e32 v24, v24
	v_add_f32_e32 v23, v58, v14
	v_med3_f32 v23, v23, s61, v214
	v_add_f32_e32 v24, 1.0, v24
	v_rcp_f32_e32 v24, v24
	s_nop 0
	v_mul_f32_e32 v18, v18, v24
	v_mul_f32_e32 v23, v23, v18
	v_add_f32_e32 v18, v54, v2
	v_min_f32_e32 v18, 0x40e00000, v18
	v_mul_f32_e32 v25, 0x3fd9db23, v18
	v_mul_f32_e32 v25, 0xbfb8aa3b, v25
	v_exp_f32_e32 v25, v25
	v_add_f32_e32 v24, v50, v10
	v_med3_f32 v24, v24, s61, v214
	v_add_f32_e32 v25, 1.0, v25
	v_rcp_f32_e32 v25, v25
	s_nop 0
	v_mul_f32_e32 v18, v18, v25
	v_mul_f32_e32 v24, v24, v18
	v_add_f32_e32 v18, v63, v7
	v_min_f32_e32 v18, 0x40e00000, v18
	v_mul_f32_e32 v26, 0x3fd9db23, v18
	v_mul_f32_e32 v26, 0xbfb8aa3b, v26
	v_exp_f32_e32 v26, v26
	v_add_f32_e32 v25, v59, v15
	v_med3_f32 v25, v25, s61, v214
	v_add_f32_e32 v26, 1.0, v26
	v_rcp_f32_e32 v26, v26
	s_nop 0
	v_mul_f32_e32 v18, v18, v26
	v_mul_f32_e32 v25, v25, v18
	v_add_f32_e32 v18, v55, v3
	v_min_f32_e32 v18, 0x40e00000, v18
	v_mul_f32_e32 v27, 0x3fd9db23, v18
	v_mul_f32_e32 v27, 0xbfb8aa3b, v27
	v_exp_f32_e32 v27, v27
	v_add_f32_e32 v26, v51, v11
	v_med3_f32 v26, v26, s61, v214
	v_add_f32_e32 v27, 1.0, v27
	v_rcp_f32_e32 v27, v27
	s_nop 0
	v_mul_f32_e32 v18, v18, v27
	v_mul_f32_e32 v26, v26, v18
	v_mov_b32_e32 v18, v113
	v_cvt_pk_fp8_f32 v18, v19, v21
	v_mov_b32_e32 v19, v113
	v_cvt_pk_fp8_f32 v19, v20, v22
	v_add_co_u32_e32 v20, vcc, s21, v16
	v_cvt_pk_fp8_f32 v18, v23, v25 op_sel:[0,0,1]
	v_cvt_pk_fp8_f32 v19, v24, v26 op_sel:[0,0,1]
	v_addc_co_u32_e32 v21, vcc, 0, v17, vcc
	s_mov_b32 s21, s20
	global_store_dwordx2 v[20:21], v[18:19], off
	v_mul_f32_e32 v18, 0x3fd9db23, v4
	v_mul_f32_e32 v18, 0xbfb8aa3b, v18
	v_exp_f32_e32 v18, v18
	s_nop 0
	v_add_f32_e32 v18, 1.0, v18
	v_rcp_f32_e32 v18, v18
	s_nop 0
	v_mul_f32_e32 v4, v4, v18
	v_mul_f32_e32 v4, v12, v4
	v_mul_f32_e32 v12, 0x3fd9db23, v0
	v_mul_f32_e32 v12, 0xbfb8aa3b, v12
	v_exp_f32_e32 v12, v12
	s_nop 0
	v_add_f32_e32 v12, 1.0, v12
	v_rcp_f32_e32 v12, v12
	s_nop 0
	v_mul_f32_e32 v0, v0, v12
	v_mul_f32_e32 v8, v8, v0
	v_add_f32_e32 v0, v45, v5
	v_min_f32_e32 v0, 0x40e00000, v0
	v_mul_f32_e32 v12, 0x3fd9db23, v0
	v_mul_f32_e32 v12, 0xbfb8aa3b, v12
	v_exp_f32_e32 v12, v12
	v_add_f32_e32 v5, v41, v13
	v_med3_f32 v5, v5, s61, v214
	v_add_f32_e32 v12, 1.0, v12
	v_rcp_f32_e32 v12, v12
	s_nop 0
	v_mul_f32_e32 v0, v0, v12
	v_mul_f32_e32 v5, v5, v0
	v_add_f32_e32 v0, v37, v1
	v_min_f32_e32 v0, 0x40e00000, v0
	v_add_f32_e32 v1, v33, v9
	v_mul_f32_e32 v9, 0x3fd9db23, v0
	v_mul_f32_e32 v9, 0xbfb8aa3b, v9
	v_exp_f32_e32 v9, v9
	v_med3_f32 v1, v1, s61, v214
	v_add_f32_e32 v9, 1.0, v9
	v_rcp_f32_e32 v9, v9
	s_nop 0
	v_mul_f32_e32 v0, v0, v9
	v_mul_f32_e32 v9, v1, v0
	v_add_f32_e32 v0, v46, v6
	v_min_f32_e32 v0, 0x40e00000, v0
	v_mul_f32_e32 v6, 0x3fd9db23, v0
	v_mul_f32_e32 v6, 0xbfb8aa3b, v6
	v_exp_f32_e32 v6, v6
	v_add_f32_e32 v1, v42, v14
	v_med3_f32 v1, v1, s61, v214
	v_add_f32_e32 v6, 1.0, v6
	v_rcp_f32_e32 v6, v6
	s_nop 0
	v_mul_f32_e32 v0, v0, v6
	v_mul_f32_e32 v1, v1, v0
	v_add_f32_e32 v0, v38, v2
	v_min_f32_e32 v0, 0x40e00000, v0
	v_mul_f32_e32 v6, 0x3fd9db23, v0
	v_mul_f32_e32 v6, 0xbfb8aa3b, v6
	v_exp_f32_e32 v6, v6
	v_add_f32_e32 v2, v34, v10
	v_med3_f32 v2, v2, s61, v214
	v_add_f32_e32 v6, 1.0, v6
	v_rcp_f32_e32 v6, v6
	s_nop 0
	v_mul_f32_e32 v0, v0, v6
	v_mul_f32_e32 v2, v2, v0
	v_add_f32_e32 v0, v47, v7
	v_min_f32_e32 v0, 0x40e00000, v0
	v_mul_f32_e32 v7, 0x3fd9db23, v0
	v_mul_f32_e32 v7, 0xbfb8aa3b, v7
	v_exp_f32_e32 v7, v7
	v_add_f32_e32 v6, v43, v15
	v_med3_f32 v6, v6, s61, v214
	v_add_f32_e32 v7, 1.0, v7
	v_rcp_f32_e32 v7, v7
	s_nop 0
	v_mul_f32_e32 v0, v0, v7
	v_mul_f32_e32 v6, v6, v0
	v_add_f32_e32 v0, v39, v3
	v_min_f32_e32 v0, 0x40e00000, v0
	v_mul_f32_e32 v7, 0x3fd9db23, v0
	v_mul_f32_e32 v7, 0xbfb8aa3b, v7
	v_exp_f32_e32 v7, v7
	v_add_f32_e32 v3, v35, v11
	v_med3_f32 v3, v3, s61, v214
	v_add_f32_e32 v7, 1.0, v7
	v_rcp_f32_e32 v7, v7
	s_nop 0
	v_mul_f32_e32 v0, v0, v7
	v_mul_f32_e32 v3, v3, v0
	v_mov_b32_e32 v0, v113
	v_cvt_pk_fp8_f32 v0, v4, v5
	v_cvt_pk_fp8_f32 v0, v1, v6 op_sel:[0,0,1]
	v_mov_b32_e32 v1, v113
	v_cvt_pk_fp8_f32 v1, v8, v9
	v_cvt_pk_fp8_f32 v1, v2, v3 op_sel:[0,0,1]
	v_add_co_u32_e32 v2, vcc, 0x2c000, v16
	s_nop 1
	v_addc_co_u32_e32 v3, vcc, 0, v17, vcc
	s_and_b64 vcc, exec, s[38:39]
	global_store_dwordx2 v[2:3], v[0:1], off
	s_cbranch_vccnz .LBB0_1081
	s_andn2_b64 vcc, exec, s[26:27]
	s_cbranch_vccnz .LBB0_1080
	s_barrier
	s_branch .LBB0_1080

.LBB0_1169:
	v_mov_b32_e32 v16, v182
	s_lshl_b32 s30, s26, 8
	v_readfirstlane_b32 s27, v16
	s_lshr_b32 s31, s27, 1
	s_and_b32 s31, s31, 0x60
	s_or_b32 s30, s31, s30
	v_lshrrev_b32_e32 v0, 1, v16
	s_ashr_i32 s27, s27, 2
	v_and_or_b32 v18, v0, 24, s30
	s_lshl_b32 s30, s36, 8
	s_andn2_b32 s27, s27, 63
	v_ashrrev_i32_e32 v173, 31, v172
	s_add_i32 s27, s27, s30
	v_lshlrev_b64 v[0:1], 12, v[172:173]
	v_and_or_b32 v16, v16, 15, s27
	v_readlane_b32 s30, v254, 24
	v_lshl_add_u64 v[0:1], s[40:41], 0, v[0:1]
	v_ashrrev_i32_e32 v19, 31, v18
	v_ashrrev_i32_e32 v17, 31, v16
	v_readlane_b32 s31, v254, 25
	v_lshl_add_u64 v[4:5], v[18:19], 2, v[0:1]
	global_load_dwordx4 v[8:11], v[4:5], off offset:16
	global_load_dwordx4 v[12:15], v[4:5], off
	global_load_dwordx4 v[0:3], v[4:5], off offset:528
	s_nop 0
	global_load_dwordx4 v[4:7], v[4:5], off offset:512
	v_lshl_add_u64 v[24:25], v[16:17], 2, s[30:31]
	global_load_dword v30, v[24:25], off
	v_or_b32_e32 v26, 16, v16
	v_ashrrev_i32_e32 v27, 31, v26
	v_lshl_add_u64 v[20:21], v[26:27], 2, s[30:31]
	global_load_dword v178, v[20:21], off
	v_or_b32_e32 v22, 32, v16
	v_ashrrev_i32_e32 v23, 31, v22
	v_lshl_add_u64 v[20:21], v[22:23], 2, s[30:31]
	global_load_dword v177, v[20:21], off
	v_or_b32_e32 v20, 48, v16
	v_ashrrev_i32_e32 v21, 31, v20
	v_lshl_add_u64 v[28:29], v[20:21], 2, s[30:31]
	global_load_dword v176, v[28:29], off
	global_load_dword v175, v[24:25], off offset:512
	global_load_dword v174, v[24:25], off offset:576
	global_load_dword v173, v[24:25], off offset:640
	global_load_dword v172, v[24:25], off offset:704
	v_lshlrev_b64 v[22:23], 10, v[22:23]
	v_lshl_add_u64 v[22:23], s[16:17], 0, v[22:23]
	v_lshl_add_u64 v[22:23], v[22:23], 0, v[18:19]
	v_lshlrev_b64 v[16:17], 10, v[16:17]
	v_lshlrev_b64 v[20:21], 10, v[20:21]
	v_lshl_add_u64 v[16:17], s[16:17], 0, v[16:17]
	v_lshl_add_u64 v[20:21], s[16:17], 0, v[20:21]
	v_lshl_add_u64 v[16:17], v[16:17], 0, v[18:19]
	s_mov_b64 s[30:31], 0x20000
	s_mov_b32 s21, 0x24000
	s_mov_b32 s27, 0x2c000
	s_mov_b64 s[50:51], -1
	v_readlane_b32 s58, v255, 15
	v_readlane_b32 s76, v255, 16
	v_readlane_b32 s77, v255, 18
	s_waitcnt vmcnt(0)
	v_pk_add_f32 v[156:157], v[156:157], v[10:11]
	v_pk_add_f32 v[28:29], v[160:161], v[14:15]
	v_pk_add_f32 v[154:155], v[154:155], v[8:9]
	v_pk_add_f32 v[148:149], v[148:149], v[2:3]
	v_pk_add_f32 v[146:147], v[146:147], v[0:1]
	v_mul_f32_e32 v24, 0x41800000, v30
	v_pk_add_f32 v[30:31], v[158:159], v[12:13]
	v_mov_b32_e32 v158, v113
	v_pk_mul_f32 v[30:31], v[30:31], v[24:25] op_sel_hi:[1,0]
	v_pk_mul_f32 v[28:29], v[28:29], v[24:25] op_sel_hi:[1,0]
	v_cvt_pk_fp8_f32 v158, v30, v31
	v_pk_add_f32 v[30:31], v[150:151], v[4:5]
	v_pk_mul_f32 v[156:157], v[156:157], v[24:25] op_sel_hi:[1,0]
	v_pk_mul_f32 v[154:155], v[154:155], v[24:25] op_sel_hi:[1,0]
	v_cvt_pk_fp8_f32 v158, v28, v29 op_sel:[0,0,1]
	v_pk_add_f32 v[28:29], v[152:153], v[6:7]
	v_pk_mul_f32 v[30:31], v[30:31], v[24:25] op_sel_hi:[1,0]
	v_pk_mul_f32 v[28:29], v[28:29], v[24:25] op_sel_hi:[1,0]
	v_pk_mul_f32 v[148:149], v[148:149], v[24:25] op_sel_hi:[1,0]
	v_pk_mul_f32 v[24:25], v[146:147], v[24:25] op_sel_hi:[1,0]
	v_mov_b32_e32 v146, v113
	v_cvt_pk_fp8_f32 v146, v30, v31
	v_pk_add_f32 v[30:31], v[142:143], v[12:13]
	v_mov_b32_e32 v142, v113
	v_mov_b32_e32 v147, v113
	v_cvt_pk_fp8_f32 v146, v28, v29 op_sel:[0,0,1]
	v_mul_f32_e32 v28, 0x41800000, v178
	v_pk_mul_f32 v[30:31], v[30:31], v[28:29] op_sel_hi:[1,0]
	v_cvt_pk_fp8_f32 v147, v24, v25
	v_cvt_pk_fp8_f32 v142, v30, v31
	v_lshlrev_b64 v[24:25], 10, v[26:27]
	v_pk_add_f32 v[26:27], v[144:145], v[14:15]
	v_pk_add_f32 v[140:141], v[140:141], v[10:11]
	v_pk_mul_f32 v[26:27], v[26:27], v[28:29] op_sel_hi:[1,0]
	v_pk_add_f32 v[138:139], v[138:139], v[8:9]
	v_cvt_pk_fp8_f32 v142, v26, v27 op_sel:[0,0,1]
	v_pk_add_f32 v[26:27], v[136:137], v[6:7]
	v_pk_add_f32 v[134:135], v[134:135], v[4:5]
	v_pk_mul_f32 v[30:31], v[26:27], v[28:29] op_sel_hi:[1,0]
	v_pk_add_f32 v[26:27], v[132:133], v[2:3]
	v_pk_add_f32 v[130:131], v[130:131], v[0:1]
	v_pk_mul_f32 v[140:141], v[140:141], v[28:29] op_sel_hi:[1,0]
	v_pk_mul_f32 v[138:139], v[138:139], v[28:29] op_sel_hi:[1,0]
	v_mov_b32_e32 v143, v113
	v_pk_mul_f32 v[134:135], v[134:135], v[28:29] op_sel_hi:[1,0]
	v_pk_mul_f32 v[26:27], v[26:27], v[28:29] op_sel_hi:[1,0]
	v_pk_mul_f32 v[28:29], v[130:131], v[28:29] op_sel_hi:[1,0]
	v_mov_b32_e32 v130, v113
	v_mov_b32_e32 v131, v113
	v_cvt_pk_fp8_f32 v143, v138, v139
	v_cvt_pk_fp8_f32 v130, v134, v135
	v_cvt_pk_fp8_f32 v131, v28, v29
	v_lshl_add_u64 v[24:25], s[16:17], 0, v[24:25]
	v_cvt_pk_fp8_f32 v143, v140, v141 op_sel:[0,0,1]
	v_cvt_pk_fp8_f32 v130, v30, v31 op_sel:[0,0,1]
	v_cvt_pk_fp8_f32 v131, v26, v27 op_sel:[0,0,1]
	v_lshl_add_u64 v[24:25], v[24:25], 0, v[18:19]
	global_store_dwordx2 v[24:25], v[142:143], off
	v_pk_add_f32 v[28:29], v[126:127], v[12:13]
	global_store_dwordx2 v[24:25], v[130:131], off offset:128
	v_mul_f32_e32 v24, 0x41800000, v177
	v_pk_add_f32 v[122:123], v[122:123], v[8:9]
	v_pk_mul_f32 v[28:29], v[28:29], v[24:25] op_sel_hi:[1,0]
	v_pk_add_f32 v[30:31], v[124:125], v[10:11]
	v_pk_mul_f32 v[122:123], v[122:123], v[24:25] op_sel_hi:[1,0]
	v_mov_b32_e32 v124, v113
	v_mov_b32_e32 v125, v113
	v_cvt_pk_fp8_f32 v124, v28, v29
	v_cvt_pk_fp8_f32 v125, v122, v123
	v_pk_add_f32 v[26:27], v[128:129], v[14:15]
	v_pk_mul_f32 v[30:31], v[30:31], v[24:25] op_sel_hi:[1,0]
	v_pk_mul_f32 v[26:27], v[26:27], v[24:25] op_sel_hi:[1,0]
	v_cvt_pk_fp8_f32 v125, v30, v31 op_sel:[0,0,1]
	v_cvt_pk_fp8_f32 v124, v26, v27 op_sel:[0,0,1]
	v_pk_add_f32 v[26:27], v[120:121], v[6:7]
	v_pk_add_f32 v[28:29], v[118:119], v[4:5]
	v_pk_add_f32 v[30:31], v[116:117], v[2:3]
	v_pk_add_f32 v[114:115], v[114:115], v[0:1]
	v_pk_mul_f32 v[26:27], v[26:27], v[24:25] op_sel_hi:[1,0]
	v_pk_mul_f32 v[28:29], v[28:29], v[24:25] op_sel_hi:[1,0]
	v_pk_mul_f32 v[30:31], v[30:31], v[24:25] op_sel_hi:[1,0]
	v_pk_mul_f32 v[24:25], v[114:115], v[24:25] op_sel_hi:[1,0]
	v_mov_b32_e32 v114, v113
	v_mov_b32_e32 v115, v113
	v_cvt_pk_fp8_f32 v114, v28, v29
	v_cvt_pk_fp8_f32 v115, v24, v25
	global_store_dwordx2 v[22:23], v[124:125], off
	v_pk_add_f32 v[24:25], v[108:109], v[12:13]
	v_cvt_pk_fp8_f32 v114, v26, v27 op_sel:[0,0,1]
	v_cvt_pk_fp8_f32 v115, v30, v31 op_sel:[0,0,1]
	v_pk_add_f32 v[28:29], v[104:105], v[8:9]
	v_mov_b32_e32 v30, v113
	v_mov_b32_e32 v31, v113
	global_store_dwordx2 v[22:23], v[114:115], off offset:128
	v_mul_f32_e32 v22, 0x41800000, v176
	v_pk_mul_f32 v[24:25], v[24:25], v[22:23] op_sel_hi:[1,0]
	v_pk_mul_f32 v[28:29], v[28:29], v[22:23] op_sel_hi:[1,0]
	v_cvt_pk_fp8_f32 v30, v24, v25
	v_cvt_pk_fp8_f32 v31, v28, v29
	v_lshl_add_u64 v[18:19], v[20:21], 0, v[18:19]
	v_pk_add_f32 v[20:21], v[110:111], v[14:15]
	v_pk_add_f32 v[26:27], v[106:107], v[10:11]
	v_pk_mul_f32 v[20:21], v[20:21], v[22:23] op_sel_hi:[1,0]
	v_pk_mul_f32 v[26:27], v[26:27], v[22:23] op_sel_hi:[1,0]
	v_cvt_pk_fp8_f32 v30, v20, v21 op_sel:[0,0,1]
	v_cvt_pk_fp8_f32 v31, v26, v27 op_sel:[0,0,1]
	v_pk_add_f32 v[20:21], v[102:103], v[6:7]
	v_pk_add_f32 v[24:25], v[100:101], v[4:5]
	v_pk_add_f32 v[26:27], v[98:99], v[2:3]
	v_pk_add_f32 v[28:29], v[96:97], v[0:1]
	v_pk_mul_f32 v[20:21], v[20:21], v[22:23] op_sel_hi:[1,0]
	v_pk_mul_f32 v[24:25], v[24:25], v[22:23] op_sel_hi:[1,0]
	v_pk_mul_f32 v[26:27], v[26:27], v[22:23] op_sel_hi:[1,0]
	v_pk_mul_f32 v[22:23], v[28:29], v[22:23] op_sel_hi:[1,0]
	v_mov_b32_e32 v28, v113
	v_mov_b32_e32 v29, v113
	v_cvt_pk_fp8_f32 v28, v24, v25
	v_cvt_pk_fp8_f32 v29, v22, v23
	global_store_dwordx2 v[18:19], v[30:31], off
	v_pk_add_f32 v[24:25], v[92:93], v[12:13]
	v_cvt_pk_fp8_f32 v28, v20, v21 op_sel:[0,0,1]
	v_cvt_pk_fp8_f32 v29, v26, v27 op_sel:[0,0,1]
	v_mov_b32_e32 v30, v113
	v_mov_b32_e32 v31, v113
	v_pk_add_f32 v[22:23], v[94:95], v[14:15]
	global_store_dwordx2 v[18:19], v[28:29], off offset:128
	v_mul_f32_e32 v18, 0x41800000, v175
	v_pk_add_f32 v[28:29], v[88:89], v[8:9]
	v_pk_mul_f32 v[24:25], v[24:25], v[18:19] op_sel_hi:[1,0]
	v_pk_mul_f32 v[28:29], v[28:29], v[18:19] op_sel_hi:[1,0]
	v_cvt_pk_fp8_f32 v30, v24, v25
	v_cvt_pk_fp8_f32 v31, v28, v29
	v_pk_add_f32 v[26:27], v[90:91], v[10:11]
	v_pk_mul_f32 v[22:23], v[22:23], v[18:19] op_sel_hi:[1,0]
	v_pk_mul_f32 v[26:27], v[26:27], v[18:19] op_sel_hi:[1,0]
	v_cvt_pk_fp8_f32 v30, v22, v23 op_sel:[0,0,1]
	v_cvt_pk_fp8_f32 v31, v26, v27 op_sel:[0,0,1]
	v_add_co_u32_e32 v22, vcc, s63, v16
	v_pk_add_f32 v[24:25], v[84:85], v[4:5]
	s_nop 0
	v_addc_co_u32_e32 v23, vcc, 0, v17, vcc
	global_store_dwordx2 v[22:23], v[30:31], off
	v_pk_add_f32 v[22:23], v[86:87], v[6:7]
	v_pk_add_f32 v[26:27], v[82:83], v[2:3]
	v_pk_add_f32 v[28:29], v[80:81], v[0:1]
	v_pk_mul_f32 v[22:23], v[22:23], v[18:19] op_sel_hi:[1,0]
	v_pk_mul_f32 v[24:25], v[24:25], v[18:19] op_sel_hi:[1,0]
	v_pk_mul_f32 v[26:27], v[26:27], v[18:19] op_sel_hi:[1,0]
	v_pk_mul_f32 v[18:19], v[28:29], v[18:19] op_sel_hi:[1,0]
	v_mov_b32_e32 v28, v113
	v_mov_b32_e32 v29, v113
	v_cvt_pk_fp8_f32 v28, v24, v25
	v_cvt_pk_fp8_f32 v29, v18, v19
	v_lshl_add_u64 v[20:21], v[16:17], 0, s[30:31]
	v_mul_f32_e32 v18, 0x41800000, v174
	v_cvt_pk_fp8_f32 v28, v22, v23 op_sel:[0,0,1]
	v_cvt_pk_fp8_f32 v29, v26, v27 op_sel:[0,0,1]
	v_pk_add_f32 v[24:25], v[76:77], v[12:13]
	v_mov_b32_e32 v30, v113
	v_pk_mul_f32 v[24:25], v[24:25], v[18:19] op_sel_hi:[1,0]
	global_store_dwordx2 v[20:21], v[28:29], off offset:128
	v_pk_add_f32 v[28:29], v[72:73], v[8:9]
	v_mov_b32_e32 v31, v113
	v_pk_mul_f32 v[28:29], v[28:29], v[18:19] op_sel_hi:[1,0]
	v_cvt_pk_fp8_f32 v30, v24, v25
	v_cvt_pk_fp8_f32 v31, v28, v29
	v_pk_add_f32 v[22:23], v[78:79], v[14:15]
	v_pk_add_f32 v[26:27], v[74:75], v[10:11]
	v_pk_mul_f32 v[22:23], v[22:23], v[18:19] op_sel_hi:[1,0]
	v_pk_mul_f32 v[26:27], v[26:27], v[18:19] op_sel_hi:[1,0]
	v_cvt_pk_fp8_f32 v30, v22, v23 op_sel:[0,0,1]
	v_cvt_pk_fp8_f32 v31, v26, v27 op_sel:[0,0,1]
	v_add_co_u32_e32 v22, vcc, s21, v16
	v_pk_add_f32 v[24:25], v[68:69], v[4:5]
	s_nop 0
	v_addc_co_u32_e32 v23, vcc, 0, v17, vcc
	global_store_dwordx2 v[22:23], v[30:31], off
	v_pk_add_f32 v[22:23], v[70:71], v[6:7]
	v_pk_add_f32 v[26:27], v[66:67], v[2:3]
	v_pk_add_f32 v[28:29], v[64:65], v[0:1]
	v_pk_mul_f32 v[22:23], v[22:23], v[18:19] op_sel_hi:[1,0]
	v_pk_mul_f32 v[24:25], v[24:25], v[18:19] op_sel_hi:[1,0]
	v_pk_mul_f32 v[26:27], v[26:27], v[18:19] op_sel_hi:[1,0]
	v_pk_mul_f32 v[18:19], v[28:29], v[18:19] op_sel_hi:[1,0]
	v_mov_b32_e32 v28, v113
	v_mov_b32_e32 v29, v113
	v_cvt_pk_fp8_f32 v28, v24, v25
	v_cvt_pk_fp8_f32 v29, v18, v19
	s_mov_b64 s[30:31], 0x24000
	v_lshl_add_u64 v[20:21], v[16:17], 0, s[30:31]
	v_cvt_pk_fp8_f32 v28, v22, v23 op_sel:[0,0,1]
	v_cvt_pk_fp8_f32 v29, v26, v27 op_sel:[0,0,1]
	v_mul_f32_e32 v18, 0x41800000, v173
	v_pk_add_f32 v[24:25], v[60:61], v[12:13]
	v_mov_b32_e32 v30, v113
	global_store_dwordx2 v[20:21], v[28:29], off offset:128
	v_pk_add_f32 v[28:29], v[56:57], v[8:9]
	v_pk_mul_f32 v[24:25], v[24:25], v[18:19] op_sel_hi:[1,0]
	v_pk_mul_f32 v[28:29], v[28:29], v[18:19] op_sel_hi:[1,0]
	v_mov_b32_e32 v31, v113
	v_cvt_pk_fp8_f32 v30, v24, v25
	v_cvt_pk_fp8_f32 v31, v28, v29
	v_pk_add_f32 v[22:23], v[62:63], v[14:15]
	v_pk_add_f32 v[26:27], v[58:59], v[10:11]
	v_pk_mul_f32 v[22:23], v[22:23], v[18:19] op_sel_hi:[1,0]
	v_pk_mul_f32 v[26:27], v[26:27], v[18:19] op_sel_hi:[1,0]
	v_cvt_pk_fp8_f32 v30, v22, v23 op_sel:[0,0,1]
	v_cvt_pk_fp8_f32 v31, v26, v27 op_sel:[0,0,1]
	s_mov_b32 s21, 0x28000
	v_add_co_u32_e32 v22, vcc, s21, v16
	v_pk_add_f32 v[24:25], v[52:53], v[4:5]
	s_nop 0
	v_addc_co_u32_e32 v23, vcc, 0, v17, vcc
	global_store_dwordx2 v[22:23], v[30:31], off
	v_pk_add_f32 v[22:23], v[54:55], v[6:7]
	v_pk_add_f32 v[26:27], v[50:51], v[2:3]
	v_pk_add_f32 v[28:29], v[48:49], v[0:1]
	v_pk_mul_f32 v[22:23], v[22:23], v[18:19] op_sel_hi:[1,0]
	v_pk_mul_f32 v[24:25], v[24:25], v[18:19] op_sel_hi:[1,0]
	v_pk_mul_f32 v[26:27], v[26:27], v[18:19] op_sel_hi:[1,0]
	v_pk_mul_f32 v[18:19], v[28:29], v[18:19] op_sel_hi:[1,0]
	v_mov_b32_e32 v28, v113
	v_cvt_pk_fp8_f32 v28, v24, v25
	v_mov_b32_e32 v29, v113
	v_cvt_pk_fp8_f32 v29, v18, v19
	v_mul_f32_e32 v18, 0x41800000, v172
	v_pk_add_f32 v[12:13], v[44:45], v[12:13]
	v_pk_add_f32 v[8:9], v[40:41], v[8:9]
	v_cvt_pk_fp8_f32 v28, v22, v23 op_sel:[0,0,1]
	v_pk_mul_f32 v[12:13], v[12:13], v[18:19] op_sel_hi:[1,0]
	v_pk_mul_f32 v[8:9], v[8:9], v[18:19] op_sel_hi:[1,0]
	v_mov_b32_e32 v22, v113
	v_mov_b32_e32 v23, v113
	v_cvt_pk_fp8_f32 v22, v12, v13
	v_cvt_pk_fp8_f32 v23, v8, v9
	v_pk_add_f32 v[14:15], v[46:47], v[14:15]
	v_pk_add_f32 v[10:11], v[42:43], v[10:11]
	v_pk_mul_f32 v[14:15], v[14:15], v[18:19] op_sel_hi:[1,0]
	v_pk_mul_f32 v[10:11], v[10:11], v[18:19] op_sel_hi:[1,0]
	v_cvt_pk_fp8_f32 v22, v14, v15 op_sel:[0,0,1]
	v_cvt_pk_fp8_f32 v23, v10, v11 op_sel:[0,0,1]
	v_add_co_u32_e32 v8, vcc, s27, v16
	v_pk_add_f32 v[4:5], v[36:37], v[4:5]
	s_nop 0
	v_addc_co_u32_e32 v9, vcc, 0, v17, vcc
	v_pk_add_f32 v[0:1], v[32:33], v[0:1]
	v_mov_b32_e32 v159, v113
	global_store_dwordx2 v[8:9], v[22:23], off
	v_pk_mul_f32 v[4:5], v[4:5], v[18:19] op_sel_hi:[1,0]
	v_pk_mul_f32 v[0:1], v[0:1], v[18:19] op_sel_hi:[1,0]
	v_mov_b32_e32 v8, v113
	v_mov_b32_e32 v9, v113
	v_cvt_pk_fp8_f32 v159, v154, v155
	v_cvt_pk_fp8_f32 v8, v4, v5
	v_cvt_pk_fp8_f32 v9, v0, v1
	v_pk_add_f32 v[6:7], v[38:39], v[6:7]
	v_pk_add_f32 v[2:3], v[34:35], v[2:3]
	v_cvt_pk_fp8_f32 v29, v26, v27 op_sel:[0,0,1]
	v_pk_mul_f32 v[6:7], v[6:7], v[18:19] op_sel_hi:[1,0]
	v_pk_mul_f32 v[2:3], v[2:3], v[18:19] op_sel_hi:[1,0]
	v_cvt_pk_fp8_f32 v159, v156, v157 op_sel:[0,0,1]
	v_cvt_pk_fp8_f32 v147, v148, v149 op_sel:[0,0,1]
	v_cvt_pk_fp8_f32 v8, v6, v7 op_sel:[0,0,1]
	v_cvt_pk_fp8_f32 v9, v2, v3 op_sel:[0,0,1]
	s_mov_b64 s[30:31], 0x28000
	v_lshl_add_u64 v[20:21], v[16:17], 0, s[30:31]
	s_mov_b64 s[30:31], 0x2c000
	global_store_dwordx2 v[20:21], v[28:29], off offset:128
	v_lshl_add_u64 v[20:21], v[16:17], 0, s[30:31]
	s_and_b64 vcc, exec, s[38:39]
	global_store_dwordx2 v[16:17], v[158:159], off
	global_store_dwordx2 v[16:17], v[146:147], off offset:128
	global_store_dwordx2 v[20:21], v[8:9], off offset:128
	s_cbranch_vccnz .LBB0_1160
	s_andn2_b64 vcc, exec, s[28:29]
	s_cbranch_vccnz .LBB0_1159
	s_barrier
	s_branch .LBB0_1159
